# v30 + K-loop MFMA segments without the redundant lgkmcnt(0) and the mid setprio pair, padded behind every loop to v30's placement modulo 64
# baseline (speedup 1.0000x reference)
.LBB0_119:
	ds_read_b128 v[148:151], v153
	ds_read_b128 v[156:159], v153 offset:1024
	ds_read_b128 v[160:163], v153 offset:2048
	ds_read_b128 v[164:167], v153 offset:3072
	ds_read_b128 v[168:171], v154
	ds_read_b128 v[172:175], v154 offset:1024
	ds_read_b128 v[176:179], v154 offset:2048
	ds_read_b128 v[180:183], v154 offset:3072
	s_add_u32 s24, s22, 0xfff80080
	s_addc_u32 s25, s23, -1
	s_cmp_eq_u32 s79, 28
	s_cselect_b32 s27, s15, s25
	s_cselect_b32 s26, s75, s24
	s_cselect_b32 s25, s13, s78
	s_cselect_b32 s24, s76, s77
	s_add_i32 m0, s21, 0xc000
	ds_read_b128 v[184:187], v155
	ds_read_b128 v[188:191], v155 offset:1024
	ds_read_b128 v[192:195], v155 offset:2048
	ds_read_b128 v[196:199], v155 offset:3072
	ds_read_b128 v[200:203], v155 offset:4096
	ds_read_b128 v[204:207], v155 offset:5120
	ds_read_b128 v[208:211], v155 offset:6144
	ds_read_b128 v[212:215], v155 offset:7168
	global_load_lds_dwordx4 v140, s[22:23]
	s_add_i32 m0, s21, 0xe000
	s_nop 0
	global_load_lds_dwordx4 v142, s[22:23]
	s_waitcnt vmcnt(8)
	s_waitcnt lgkmcnt(0)
	s_barrier
	s_setprio 1
	v_mfma_f32_16x16x32_bf16 v[126:129], v[148:151], v[184:187], v[126:129]
	v_mfma_f32_16x16x32_bf16 v[122:125], v[160:163], v[184:187], v[122:125]
	v_mfma_f32_16x16x32_bf16 v[118:121], v[148:151], v[192:195], v[118:121]
	v_mfma_f32_16x16x32_bf16 v[110:113], v[160:163], v[192:195], v[110:113]
	v_mfma_f32_16x16x32_bf16 v[102:105], v[148:151], v[200:203], v[102:105]
	v_mfma_f32_16x16x32_bf16 v[94:97], v[160:163], v[200:203], v[94:97]
	v_mfma_f32_16x16x32_bf16 v[86:89], v[148:151], v[208:211], v[86:89]
	v_mfma_f32_16x16x32_bf16 v[78:81], v[160:163], v[208:211], v[78:81]
	v_mfma_f32_16x16x32_bf16 v[126:129], v[156:159], v[188:191], v[126:129]
	v_mfma_f32_16x16x32_bf16 v[122:125], v[164:167], v[188:191], v[122:125]
	v_mfma_f32_16x16x32_bf16 v[118:121], v[156:159], v[196:199], v[118:121]
	v_mfma_f32_16x16x32_bf16 v[110:113], v[164:167], v[196:199], v[110:113]
	v_mfma_f32_16x16x32_bf16 v[102:105], v[156:159], v[204:207], v[102:105]
	v_mfma_f32_16x16x32_bf16 v[94:97], v[164:167], v[204:207], v[94:97]
	v_mfma_f32_16x16x32_bf16 v[86:89], v[156:159], v[212:215], v[86:89]
	v_mfma_f32_16x16x32_bf16 v[78:81], v[164:167], v[212:215], v[78:81]
	v_mfma_f32_16x16x32_bf16 v[114:117], v[168:171], v[184:187], v[114:117]
	v_mfma_f32_16x16x32_bf16 v[106:109], v[176:179], v[184:187], v[106:109]
	v_mfma_f32_16x16x32_bf16 v[98:101], v[168:171], v[192:195], v[98:101]
	v_mfma_f32_16x16x32_bf16 v[90:93], v[176:179], v[192:195], v[90:93]
	v_mfma_f32_16x16x32_bf16 v[82:85], v[168:171], v[200:203], v[82:85]
	v_mfma_f32_16x16x32_bf16 v[74:77], v[176:179], v[200:203], v[74:77]
	v_mfma_f32_16x16x32_bf16 v[70:73], v[168:171], v[208:211], v[70:73]
	v_mfma_f32_16x16x32_bf16 v[66:69], v[176:179], v[208:211], v[66:69]
	v_mfma_f32_16x16x32_bf16 v[114:117], v[172:175], v[188:191], v[114:117]
	v_mfma_f32_16x16x32_bf16 v[106:109], v[180:183], v[188:191], v[106:109]
	v_mfma_f32_16x16x32_bf16 v[98:101], v[172:175], v[196:199], v[98:101]
	v_mfma_f32_16x16x32_bf16 v[90:93], v[180:183], v[196:199], v[90:93]
	v_mfma_f32_16x16x32_bf16 v[82:85], v[172:175], v[204:207], v[82:85]
	v_mfma_f32_16x16x32_bf16 v[74:77], v[180:183], v[204:207], v[74:77]
	v_mfma_f32_16x16x32_bf16 v[70:73], v[172:175], v[212:215], v[70:73]
	v_mfma_f32_16x16x32_bf16 v[66:69], v[180:183], v[212:215], v[66:69]
	s_setprio 0
	s_barrier
	s_add_i32 s80, s71, s33
	v_lshl_add_u64 v[216:217], s[24:25], 0, v[136:137]
	s_mov_b32 m0, s80
	ds_read_b128 v[184:187], v155 offset:16384
	ds_read_b128 v[188:191], v155 offset:17408
	ds_read_b128 v[192:195], v155 offset:18432
	ds_read_b128 v[196:199], v155 offset:19456
	ds_read_b128 v[200:203], v155 offset:20480
	ds_read_b128 v[204:207], v155 offset:21504
	ds_read_b128 v[208:211], v155 offset:22528
	ds_read_b128 v[212:215], v155 offset:23552
	global_load_lds_dwordx4 v136, s[24:25]
	s_add_i32 m0, s80, 0x2000
	s_add_u32 s80, s24, 0x80000
	v_lshl_add_u64 v[218:219], s[24:25], 0, v[132:133]
	s_addc_u32 s81, s25, 0
	s_add_i32 s82, s72, s33
	global_load_lds_dwordx4 v132, s[24:25]
	s_mov_b32 m0, s82
	v_lshl_add_u64 v[222:223], s[26:27], 0, v[134:135]
	global_load_lds_dwordx4 v136, s[80:81]
	s_add_i32 m0, s82, 0x2000
	s_nop 0
	global_load_lds_dwordx4 v132, s[80:81]
	v_lshl_add_u64 v[220:221], s[26:27], 0, v[138:139]
	s_mov_b32 m0, s21
	s_nop 0
	global_load_lds_dwordx4 v138, s[26:27]
	s_mov_b32 m0, s36
	s_nop 0
	global_load_lds_dwordx4 v134, s[26:27]
	s_waitcnt vmcnt(8)
	s_waitcnt lgkmcnt(0)
	s_barrier
	s_setprio 1
	v_mfma_f32_16x16x32_bf16 v[62:65], v[148:151], v[184:187], v[62:65]
	v_mfma_f32_16x16x32_bf16 v[58:61], v[160:163], v[184:187], v[58:61]
	v_mfma_f32_16x16x32_bf16 v[54:57], v[148:151], v[192:195], v[54:57]
	v_mfma_f32_16x16x32_bf16 v[46:49], v[160:163], v[192:195], v[46:49]
	v_mfma_f32_16x16x32_bf16 v[38:41], v[148:151], v[200:203], v[38:41]
	v_mfma_f32_16x16x32_bf16 v[30:33], v[160:163], v[200:203], v[30:33]
	v_mfma_f32_16x16x32_bf16 v[22:25], v[148:151], v[208:211], v[22:25]
	v_mfma_f32_16x16x32_bf16 v[14:17], v[160:163], v[208:211], v[14:17]
	v_mfma_f32_16x16x32_bf16 v[62:65], v[156:159], v[188:191], v[62:65]
	v_mfma_f32_16x16x32_bf16 v[58:61], v[164:167], v[188:191], v[58:61]
	v_mfma_f32_16x16x32_bf16 v[54:57], v[156:159], v[196:199], v[54:57]
	v_mfma_f32_16x16x32_bf16 v[46:49], v[164:167], v[196:199], v[46:49]
	v_mfma_f32_16x16x32_bf16 v[38:41], v[156:159], v[204:207], v[38:41]
	v_mfma_f32_16x16x32_bf16 v[30:33], v[164:167], v[204:207], v[30:33]
	v_mfma_f32_16x16x32_bf16 v[22:25], v[156:159], v[212:215], v[22:25]
	v_mfma_f32_16x16x32_bf16 v[14:17], v[164:167], v[212:215], v[14:17]
	v_mfma_f32_16x16x32_bf16 v[50:53], v[168:171], v[184:187], v[50:53]
	v_mfma_f32_16x16x32_bf16 v[42:45], v[176:179], v[184:187], v[42:45]
	v_mfma_f32_16x16x32_bf16 v[34:37], v[168:171], v[192:195], v[34:37]
	v_mfma_f32_16x16x32_bf16 v[26:29], v[176:179], v[192:195], v[26:29]
	v_mfma_f32_16x16x32_bf16 v[18:21], v[168:171], v[200:203], v[18:21]
	v_mfma_f32_16x16x32_bf16 v[10:13], v[176:179], v[200:203], v[10:13]
	v_mfma_f32_16x16x32_bf16 v[6:9], v[168:171], v[208:211], v[6:9]
	v_mfma_f32_16x16x32_bf16 v[2:5], v[176:179], v[208:211], v[2:5]
	v_mfma_f32_16x16x32_bf16 v[50:53], v[172:175], v[188:191], v[50:53]
	v_mfma_f32_16x16x32_bf16 v[42:45], v[180:183], v[188:191], v[42:45]
	v_mfma_f32_16x16x32_bf16 v[34:37], v[172:175], v[196:199], v[34:37]
	v_mfma_f32_16x16x32_bf16 v[26:29], v[180:183], v[196:199], v[26:29]
	v_mfma_f32_16x16x32_bf16 v[18:21], v[172:175], v[204:207], v[18:21]
	v_mfma_f32_16x16x32_bf16 v[10:13], v[180:183], v[204:207], v[10:13]
	v_mfma_f32_16x16x32_bf16 v[6:9], v[172:175], v[212:215], v[6:9]
	v_mfma_f32_16x16x32_bf16 v[2:5], v[180:183], v[212:215], v[2:5]
	s_setprio 0
	s_barrier
	s_add_i32 s80, 0, 0x18000
	s_add_i32 s81, 0, 0x1c000
	v_add_u32_e32 v164, s80, v131
	v_add_u32_e32 v180, s81, v131
	ds_read_b128 v[148:151], v164
	ds_read_b128 v[156:159], v164 offset:1024
	ds_read_b128 v[160:163], v164 offset:2048
	ds_read_b128 v[164:167], v164 offset:3072
	ds_read_b128 v[168:171], v180
	ds_read_b128 v[172:175], v180 offset:1024
	ds_read_b128 v[176:179], v180 offset:2048
	ds_read_b128 v[180:183], v180 offset:3072
	s_add_u32 s26, s26, 0x80000
	s_addc_u32 s27, s27, 0
	s_mov_b32 m0, s37
	ds_read_b128 v[184:187], v155 offset:32768
	ds_read_b128 v[188:191], v155 offset:33792
	ds_read_b128 v[192:195], v155 offset:34816
	ds_read_b128 v[196:199], v155 offset:35840
	ds_read_b128 v[200:203], v155 offset:36864
	ds_read_b128 v[204:207], v155 offset:37888
	ds_read_b128 v[208:211], v155 offset:38912
	ds_read_b128 v[212:215], v155 offset:39936
	global_load_lds_dwordx4 v138, s[26:27]
	s_mov_b32 m0, s42
	s_nop 0
	global_load_lds_dwordx4 v134, s[26:27]
	s_waitcnt vmcnt(8)
	s_waitcnt lgkmcnt(0)
	s_barrier
	s_setprio 1
	v_mfma_f32_16x16x32_bf16 v[126:129], v[148:151], v[184:187], v[126:129]
	v_mfma_f32_16x16x32_bf16 v[122:125], v[160:163], v[184:187], v[122:125]
	v_mfma_f32_16x16x32_bf16 v[118:121], v[148:151], v[192:195], v[118:121]
	v_mfma_f32_16x16x32_bf16 v[110:113], v[160:163], v[192:195], v[110:113]
	v_mfma_f32_16x16x32_bf16 v[102:105], v[148:151], v[200:203], v[102:105]
	v_mfma_f32_16x16x32_bf16 v[94:97], v[160:163], v[200:203], v[94:97]
	v_mfma_f32_16x16x32_bf16 v[86:89], v[148:151], v[208:211], v[86:89]
	v_mfma_f32_16x16x32_bf16 v[78:81], v[160:163], v[208:211], v[78:81]
	v_mfma_f32_16x16x32_bf16 v[126:129], v[156:159], v[188:191], v[126:129]
	v_mfma_f32_16x16x32_bf16 v[122:125], v[164:167], v[188:191], v[122:125]
	v_mfma_f32_16x16x32_bf16 v[118:121], v[156:159], v[196:199], v[118:121]
	v_mfma_f32_16x16x32_bf16 v[110:113], v[164:167], v[196:199], v[110:113]
	v_mfma_f32_16x16x32_bf16 v[102:105], v[156:159], v[204:207], v[102:105]
	v_mfma_f32_16x16x32_bf16 v[94:97], v[164:167], v[204:207], v[94:97]
	v_mfma_f32_16x16x32_bf16 v[86:89], v[156:159], v[212:215], v[86:89]
	v_mfma_f32_16x16x32_bf16 v[78:81], v[164:167], v[212:215], v[78:81]
	v_mfma_f32_16x16x32_bf16 v[114:117], v[168:171], v[184:187], v[114:117]
	v_mfma_f32_16x16x32_bf16 v[106:109], v[176:179], v[184:187], v[106:109]
	v_mfma_f32_16x16x32_bf16 v[98:101], v[168:171], v[192:195], v[98:101]
	v_mfma_f32_16x16x32_bf16 v[90:93], v[176:179], v[192:195], v[90:93]
	v_mfma_f32_16x16x32_bf16 v[82:85], v[168:171], v[200:203], v[82:85]
	v_mfma_f32_16x16x32_bf16 v[74:77], v[176:179], v[200:203], v[74:77]
	v_mfma_f32_16x16x32_bf16 v[70:73], v[168:171], v[208:211], v[70:73]
	v_mfma_f32_16x16x32_bf16 v[66:69], v[176:179], v[208:211], v[66:69]
	v_mfma_f32_16x16x32_bf16 v[114:117], v[172:175], v[188:191], v[114:117]
	v_mfma_f32_16x16x32_bf16 v[106:109], v[180:183], v[188:191], v[106:109]
	v_mfma_f32_16x16x32_bf16 v[98:101], v[172:175], v[196:199], v[98:101]
	v_mfma_f32_16x16x32_bf16 v[90:93], v[180:183], v[196:199], v[90:93]
	v_mfma_f32_16x16x32_bf16 v[82:85], v[172:175], v[204:207], v[82:85]
	v_mfma_f32_16x16x32_bf16 v[74:77], v[180:183], v[204:207], v[74:77]
	v_mfma_f32_16x16x32_bf16 v[70:73], v[172:175], v[212:215], v[70:73]
	v_mfma_f32_16x16x32_bf16 v[66:69], v[180:183], v[212:215], v[66:69]
	s_setprio 0
	s_barrier
	s_add_i32 s26, s80, s33
	v_lshl_add_u64 v[216:217], v[216:217], 0, s[8:9]
	s_mov_b32 m0, s26
	ds_read_b128 v[184:187], v155 offset:49152
	ds_read_b128 v[188:191], v155 offset:50176
	ds_read_b128 v[192:195], v155 offset:51200
	ds_read_b128 v[196:199], v155 offset:52224
	ds_read_b128 v[200:203], v155 offset:53248
	ds_read_b128 v[204:207], v155 offset:54272
	ds_read_b128 v[208:211], v155 offset:55296
	ds_read_b128 v[212:215], v155 offset:56320
	global_load_lds_dwordx4 v[216:217], off
	s_add_i32 m0, s26, 0x2000
	s_add_u32 s24, s24, 0x80080
	v_lshl_add_u64 v[216:217], v[218:219], 0, s[8:9]
	s_addc_u32 s25, s25, 0
	s_add_i32 s26, s81, s33
	global_load_lds_dwordx4 v[216:217], off
	s_mov_b32 m0, s26
	s_nop 0
	global_load_lds_dwordx4 v136, s[24:25]
	s_add_i32 m0, s26, 0x2000
	s_nop 0
	global_load_lds_dwordx4 v132, s[24:25]
	v_lshl_add_u64 v[216:217], v[220:221], 0, s[8:9]
	s_mov_b32 m0, s44
	s_nop 0
	global_load_lds_dwordx4 v[216:217], off
	v_lshl_add_u64 v[216:217], v[222:223], 0, s[8:9]
	s_mov_b32 m0, s45
	s_nop 0
	global_load_lds_dwordx4 v[216:217], off
	s_waitcnt vmcnt(8)
	s_waitcnt lgkmcnt(0)
	s_barrier
	s_setprio 1
	v_mfma_f32_16x16x32_bf16 v[62:65], v[148:151], v[184:187], v[62:65]
	v_mfma_f32_16x16x32_bf16 v[58:61], v[160:163], v[184:187], v[58:61]
	v_mfma_f32_16x16x32_bf16 v[54:57], v[148:151], v[192:195], v[54:57]
	v_mfma_f32_16x16x32_bf16 v[46:49], v[160:163], v[192:195], v[46:49]
	v_mfma_f32_16x16x32_bf16 v[38:41], v[148:151], v[200:203], v[38:41]
	v_mfma_f32_16x16x32_bf16 v[30:33], v[160:163], v[200:203], v[30:33]
	v_mfma_f32_16x16x32_bf16 v[22:25], v[148:151], v[208:211], v[22:25]
	v_mfma_f32_16x16x32_bf16 v[14:17], v[160:163], v[208:211], v[14:17]
	v_mfma_f32_16x16x32_bf16 v[62:65], v[156:159], v[188:191], v[62:65]
	v_mfma_f32_16x16x32_bf16 v[58:61], v[164:167], v[188:191], v[58:61]
	v_mfma_f32_16x16x32_bf16 v[54:57], v[156:159], v[196:199], v[54:57]
	v_mfma_f32_16x16x32_bf16 v[46:49], v[164:167], v[196:199], v[46:49]
	v_mfma_f32_16x16x32_bf16 v[38:41], v[156:159], v[204:207], v[38:41]
	v_mfma_f32_16x16x32_bf16 v[30:33], v[164:167], v[204:207], v[30:33]
	v_mfma_f32_16x16x32_bf16 v[22:25], v[156:159], v[212:215], v[22:25]
	v_mfma_f32_16x16x32_bf16 v[14:17], v[164:167], v[212:215], v[14:17]
	v_mfma_f32_16x16x32_bf16 v[50:53], v[168:171], v[184:187], v[50:53]
	v_mfma_f32_16x16x32_bf16 v[42:45], v[176:179], v[184:187], v[42:45]
	v_mfma_f32_16x16x32_bf16 v[34:37], v[168:171], v[192:195], v[34:37]
	v_mfma_f32_16x16x32_bf16 v[26:29], v[176:179], v[192:195], v[26:29]
	v_mfma_f32_16x16x32_bf16 v[18:21], v[168:171], v[200:203], v[18:21]
	v_mfma_f32_16x16x32_bf16 v[10:13], v[176:179], v[200:203], v[10:13]
	v_mfma_f32_16x16x32_bf16 v[6:9], v[168:171], v[208:211], v[6:9]
	v_mfma_f32_16x16x32_bf16 v[2:5], v[176:179], v[208:211], v[2:5]
	v_mfma_f32_16x16x32_bf16 v[50:53], v[172:175], v[188:191], v[50:53]
	v_mfma_f32_16x16x32_bf16 v[42:45], v[180:183], v[188:191], v[42:45]
	v_mfma_f32_16x16x32_bf16 v[34:37], v[172:175], v[196:199], v[34:37]
	v_mfma_f32_16x16x32_bf16 v[26:29], v[180:183], v[196:199], v[26:29]
	v_mfma_f32_16x16x32_bf16 v[18:21], v[172:175], v[204:207], v[18:21]
	v_mfma_f32_16x16x32_bf16 v[10:13], v[180:183], v[204:207], v[10:13]
	v_mfma_f32_16x16x32_bf16 v[6:9], v[172:175], v[212:215], v[6:9]
	v_mfma_f32_16x16x32_bf16 v[2:5], v[180:183], v[212:215], v[2:5]
	s_setprio 0
	s_barrier
	s_add_i32 s79, s79, 2
	s_add_u32 s22, s22, 0x100
	s_addc_u32 s23, s23, 0
	s_add_u32 s77, s77, 0x100
	s_addc_u32 s78, s78, 0
	s_cmp_gt_u32 s79, 29
	s_cbranch_scc0 .LBB0_119
	s_nop 0
	s_nop 0
	s_nop 0
	s_nop 0
	s_nop 0
	s_nop 0
	s_nop 0
	s_nop 0
	s_nop 0
	s_nop 0
	s_nop 0
	s_nop 0
	s_and_b64 vcc, exec, s[10:11]
	s_cbranch_vccz .LBB0_122
	s_barrier

.LBB0_466:
	ds_read_b128 v[150:153], v211
	ds_read_b128 v[154:157], v211 offset:1024
	ds_read_b128 v[158:161], v211 offset:2048
	ds_read_b128 v[162:165], v211 offset:3072
	ds_read_b128 v[166:169], v212
	ds_read_b128 v[170:173], v212 offset:1024
	ds_read_b128 v[174:177], v212 offset:2048
	ds_read_b128 v[178:181], v212 offset:3072
	s_add_u32 s42, s36, 0xfff80080
	s_addc_u32 s43, s37, -1
	s_cmp_eq_u32 s83, 28
	s_cselect_b32 s45, s1, s43
	s_cselect_b32 s44, s27, s42
	s_cselect_b32 s43, s25, s63
	s_cselect_b32 s42, s35, s62
	s_add_i32 m0, s67, 0xc000
	ds_read_b128 v[182:185], v213
	ds_read_b128 v[186:189], v213 offset:1024
	ds_read_b128 v[190:193], v213 offset:2048
	ds_read_b128 v[194:197], v213 offset:3072
	ds_read_b128 v[198:201], v213 offset:4096
	ds_read_b128 v[202:205], v213 offset:5120
	ds_read_b128 v[218:221], v213 offset:6144
	ds_read_b128 v[222:225], v213 offset:7168
	global_load_lds_dwordx4 v142, s[36:37]
	s_add_i32 m0, s67, 0xe000
	s_nop 0
	global_load_lds_dwordx4 v144, s[36:37]
	s_waitcnt vmcnt(8)
	s_waitcnt lgkmcnt(0)
	s_barrier
	s_setprio 1
	v_mfma_f32_16x16x32_bf16 v[126:129], v[150:153], v[182:185], v[126:129]
	v_mfma_f32_16x16x32_bf16 v[122:125], v[158:161], v[182:185], v[122:125]
	v_mfma_f32_16x16x32_bf16 v[110:113], v[150:153], v[190:193], v[110:113]
	v_mfma_f32_16x16x32_bf16 v[106:109], v[158:161], v[190:193], v[106:109]
	v_mfma_f32_16x16x32_bf16 v[94:97], v[150:153], v[198:201], v[94:97]
	v_mfma_f32_16x16x32_bf16 v[90:93], v[158:161], v[198:201], v[90:93]
	v_mfma_f32_16x16x32_bf16 v[78:81], v[150:153], v[218:221], v[78:81]
	v_mfma_f32_16x16x32_bf16 v[74:77], v[158:161], v[218:221], v[74:77]
	v_mfma_f32_16x16x32_bf16 v[126:129], v[154:157], v[186:189], v[126:129]
	v_mfma_f32_16x16x32_bf16 v[122:125], v[162:165], v[186:189], v[122:125]
	v_mfma_f32_16x16x32_bf16 v[110:113], v[154:157], v[194:197], v[110:113]
	v_mfma_f32_16x16x32_bf16 v[106:109], v[162:165], v[194:197], v[106:109]
	v_mfma_f32_16x16x32_bf16 v[94:97], v[154:157], v[202:205], v[94:97]
	v_mfma_f32_16x16x32_bf16 v[90:93], v[162:165], v[202:205], v[90:93]
	v_mfma_f32_16x16x32_bf16 v[78:81], v[154:157], v[222:225], v[78:81]
	v_mfma_f32_16x16x32_bf16 v[74:77], v[162:165], v[222:225], v[74:77]
	v_mfma_f32_16x16x32_bf16 v[118:121], v[166:169], v[182:185], v[118:121]
	v_mfma_f32_16x16x32_bf16 v[114:117], v[174:177], v[182:185], v[114:117]
	v_mfma_f32_16x16x32_bf16 v[102:105], v[166:169], v[190:193], v[102:105]
	v_mfma_f32_16x16x32_bf16 v[98:101], v[174:177], v[190:193], v[98:101]
	v_mfma_f32_16x16x32_bf16 v[86:89], v[166:169], v[198:201], v[86:89]
	v_mfma_f32_16x16x32_bf16 v[82:85], v[174:177], v[198:201], v[82:85]
	v_mfma_f32_16x16x32_bf16 v[70:73], v[166:169], v[218:221], v[70:73]
	v_mfma_f32_16x16x32_bf16 v[66:69], v[174:177], v[218:221], v[66:69]
	v_mfma_f32_16x16x32_bf16 v[118:121], v[170:173], v[186:189], v[118:121]
	v_mfma_f32_16x16x32_bf16 v[114:117], v[178:181], v[186:189], v[114:117]
	v_mfma_f32_16x16x32_bf16 v[102:105], v[170:173], v[194:197], v[102:105]
	v_mfma_f32_16x16x32_bf16 v[98:101], v[178:181], v[194:197], v[98:101]
	v_mfma_f32_16x16x32_bf16 v[86:89], v[170:173], v[202:205], v[86:89]
	v_mfma_f32_16x16x32_bf16 v[82:85], v[178:181], v[202:205], v[82:85]
	v_mfma_f32_16x16x32_bf16 v[70:73], v[170:173], v[222:225], v[70:73]
	v_mfma_f32_16x16x32_bf16 v[66:69], v[178:181], v[222:225], v[66:69]
	s_setprio 0
	s_barrier
	s_add_i32 s84, s79, s66
	v_lshl_add_u64 v[226:227], s[42:43], 0, v[132:133]
	s_mov_b32 m0, s84
	ds_read_b128 v[182:185], v213 offset:16384
	ds_read_b128 v[186:189], v213 offset:17408
	ds_read_b128 v[190:193], v213 offset:18432
	ds_read_b128 v[194:197], v213 offset:19456
	ds_read_b128 v[198:201], v213 offset:20480
	ds_read_b128 v[202:205], v213 offset:21504
	ds_read_b128 v[218:221], v213 offset:22528
	ds_read_b128 v[222:225], v213 offset:23552
	global_load_lds_dwordx4 v132, s[42:43]
	s_add_i32 m0, s84, 0x2000
	s_add_u32 s84, s42, 0x80000
	v_lshl_add_u64 v[228:229], s[42:43], 0, v[136:137]
	s_addc_u32 s85, s43, 0
	s_add_i32 s86, s80, s66
	global_load_lds_dwordx4 v136, s[42:43]
	s_mov_b32 m0, s86
	v_lshl_add_u64 v[232:233], s[44:45], 0, v[134:135]
	global_load_lds_dwordx4 v132, s[84:85]
	s_add_i32 m0, s86, 0x2000
	s_nop 0
	global_load_lds_dwordx4 v136, s[84:85]
	v_lshl_add_u64 v[230:231], s[44:45], 0, v[130:131]
	s_mov_b32 m0, s67
	s_nop 0
	global_load_lds_dwordx4 v130, s[44:45]
	s_mov_b32 m0, s68
	s_nop 0
	global_load_lds_dwordx4 v134, s[44:45]
	s_waitcnt vmcnt(8)
	s_waitcnt lgkmcnt(0)
	s_barrier
	s_setprio 1
	v_mfma_f32_16x16x32_bf16 v[62:65], v[150:153], v[182:185], v[62:65]
	v_mfma_f32_16x16x32_bf16 v[58:61], v[158:161], v[182:185], v[58:61]
	v_mfma_f32_16x16x32_bf16 v[46:49], v[150:153], v[190:193], v[46:49]
	v_mfma_f32_16x16x32_bf16 v[42:45], v[158:161], v[190:193], v[42:45]
	v_mfma_f32_16x16x32_bf16 v[30:33], v[150:153], v[198:201], v[30:33]
	v_mfma_f32_16x16x32_bf16 v[26:29], v[158:161], v[198:201], v[26:29]
	v_mfma_f32_16x16x32_bf16 v[14:17], v[150:153], v[218:221], v[14:17]
	v_mfma_f32_16x16x32_bf16 v[10:13], v[158:161], v[218:221], v[10:13]
	v_mfma_f32_16x16x32_bf16 v[62:65], v[154:157], v[186:189], v[62:65]
	v_mfma_f32_16x16x32_bf16 v[58:61], v[162:165], v[186:189], v[58:61]
	v_mfma_f32_16x16x32_bf16 v[46:49], v[154:157], v[194:197], v[46:49]
	v_mfma_f32_16x16x32_bf16 v[42:45], v[162:165], v[194:197], v[42:45]
	v_mfma_f32_16x16x32_bf16 v[30:33], v[154:157], v[202:205], v[30:33]
	v_mfma_f32_16x16x32_bf16 v[26:29], v[162:165], v[202:205], v[26:29]
	v_mfma_f32_16x16x32_bf16 v[14:17], v[154:157], v[222:225], v[14:17]
	v_mfma_f32_16x16x32_bf16 v[10:13], v[162:165], v[222:225], v[10:13]
	v_mfma_f32_16x16x32_bf16 v[54:57], v[166:169], v[182:185], v[54:57]
	v_mfma_f32_16x16x32_bf16 v[50:53], v[174:177], v[182:185], v[50:53]
	v_mfma_f32_16x16x32_bf16 v[38:41], v[166:169], v[190:193], v[38:41]
	v_mfma_f32_16x16x32_bf16 v[34:37], v[174:177], v[190:193], v[34:37]
	v_mfma_f32_16x16x32_bf16 v[22:25], v[166:169], v[198:201], v[22:25]
	v_mfma_f32_16x16x32_bf16 v[18:21], v[174:177], v[198:201], v[18:21]
	v_mfma_f32_16x16x32_bf16 v[6:9], v[166:169], v[218:221], v[6:9]
	v_mfma_f32_16x16x32_bf16 v[2:5], v[174:177], v[218:221], v[2:5]
	v_mfma_f32_16x16x32_bf16 v[54:57], v[170:173], v[186:189], v[54:57]
	v_mfma_f32_16x16x32_bf16 v[50:53], v[178:181], v[186:189], v[50:53]
	v_mfma_f32_16x16x32_bf16 v[38:41], v[170:173], v[194:197], v[38:41]
	v_mfma_f32_16x16x32_bf16 v[34:37], v[178:181], v[194:197], v[34:37]
	v_mfma_f32_16x16x32_bf16 v[22:25], v[170:173], v[202:205], v[22:25]
	v_mfma_f32_16x16x32_bf16 v[18:21], v[178:181], v[202:205], v[18:21]
	v_mfma_f32_16x16x32_bf16 v[6:9], v[170:173], v[222:225], v[6:9]
	v_mfma_f32_16x16x32_bf16 v[2:5], v[178:181], v[222:225], v[2:5]
	s_setprio 0
	s_barrier
	s_add_i32 s84, 0, 0x18000
	v_add_u32_e32 v139, s84, v206
	s_add_i32 s85, 0, 0x1c000
	ds_read_b128 v[150:153], v139
	ds_read_b128 v[154:157], v139 offset:1024
	ds_read_b128 v[158:161], v139 offset:2048
	ds_read_b128 v[162:165], v139 offset:3072
	v_add_u32_e32 v139, s85, v206
	ds_read_b128 v[166:169], v139
	ds_read_b128 v[170:173], v139 offset:1024
	ds_read_b128 v[174:177], v139 offset:2048
	ds_read_b128 v[178:181], v139 offset:3072
	s_add_u32 s44, s44, 0x80000
	s_addc_u32 s45, s45, 0
	s_mov_b32 m0, s69
	ds_read_b128 v[182:185], v213 offset:32768
	ds_read_b128 v[186:189], v213 offset:33792
	ds_read_b128 v[190:193], v213 offset:34816
	ds_read_b128 v[194:197], v213 offset:35840
	ds_read_b128 v[198:201], v213 offset:36864
	ds_read_b128 v[202:205], v213 offset:37888
	ds_read_b128 v[218:221], v213 offset:38912
	ds_read_b128 v[222:225], v213 offset:39936
	global_load_lds_dwordx4 v130, s[44:45]
	s_mov_b32 m0, s70
	s_nop 0
	global_load_lds_dwordx4 v134, s[44:45]
	s_waitcnt vmcnt(8)
	s_waitcnt lgkmcnt(0)
	s_barrier
	s_setprio 1
	v_mfma_f32_16x16x32_bf16 v[126:129], v[150:153], v[182:185], v[126:129]
	v_mfma_f32_16x16x32_bf16 v[122:125], v[158:161], v[182:185], v[122:125]
	v_mfma_f32_16x16x32_bf16 v[110:113], v[150:153], v[190:193], v[110:113]
	v_mfma_f32_16x16x32_bf16 v[106:109], v[158:161], v[190:193], v[106:109]
	v_mfma_f32_16x16x32_bf16 v[94:97], v[150:153], v[198:201], v[94:97]
	v_mfma_f32_16x16x32_bf16 v[90:93], v[158:161], v[198:201], v[90:93]
	v_mfma_f32_16x16x32_bf16 v[78:81], v[150:153], v[218:221], v[78:81]
	v_mfma_f32_16x16x32_bf16 v[74:77], v[158:161], v[218:221], v[74:77]
	v_mfma_f32_16x16x32_bf16 v[126:129], v[154:157], v[186:189], v[126:129]
	v_mfma_f32_16x16x32_bf16 v[122:125], v[162:165], v[186:189], v[122:125]
	v_mfma_f32_16x16x32_bf16 v[110:113], v[154:157], v[194:197], v[110:113]
	v_mfma_f32_16x16x32_bf16 v[106:109], v[162:165], v[194:197], v[106:109]
	v_mfma_f32_16x16x32_bf16 v[94:97], v[154:157], v[202:205], v[94:97]
	v_mfma_f32_16x16x32_bf16 v[90:93], v[162:165], v[202:205], v[90:93]
	v_mfma_f32_16x16x32_bf16 v[78:81], v[154:157], v[222:225], v[78:81]
	v_mfma_f32_16x16x32_bf16 v[74:77], v[162:165], v[222:225], v[74:77]
	v_mfma_f32_16x16x32_bf16 v[118:121], v[166:169], v[182:185], v[118:121]
	v_mfma_f32_16x16x32_bf16 v[114:117], v[174:177], v[182:185], v[114:117]
	v_mfma_f32_16x16x32_bf16 v[102:105], v[166:169], v[190:193], v[102:105]
	v_mfma_f32_16x16x32_bf16 v[98:101], v[174:177], v[190:193], v[98:101]
	v_mfma_f32_16x16x32_bf16 v[86:89], v[166:169], v[198:201], v[86:89]
	v_mfma_f32_16x16x32_bf16 v[82:85], v[174:177], v[198:201], v[82:85]
	v_mfma_f32_16x16x32_bf16 v[70:73], v[166:169], v[218:221], v[70:73]
	v_mfma_f32_16x16x32_bf16 v[66:69], v[174:177], v[218:221], v[66:69]
	v_mfma_f32_16x16x32_bf16 v[118:121], v[170:173], v[186:189], v[118:121]
	v_mfma_f32_16x16x32_bf16 v[114:117], v[178:181], v[186:189], v[114:117]
	v_mfma_f32_16x16x32_bf16 v[102:105], v[170:173], v[194:197], v[102:105]
	v_mfma_f32_16x16x32_bf16 v[98:101], v[178:181], v[194:197], v[98:101]
	v_mfma_f32_16x16x32_bf16 v[86:89], v[170:173], v[202:205], v[86:89]
	v_mfma_f32_16x16x32_bf16 v[82:85], v[178:181], v[202:205], v[82:85]
	v_mfma_f32_16x16x32_bf16 v[70:73], v[170:173], v[222:225], v[70:73]
	v_mfma_f32_16x16x32_bf16 v[66:69], v[178:181], v[222:225], v[66:69]
	s_setprio 0
	s_barrier
	s_add_i32 s44, s84, s66
	v_lshl_add_u64 v[226:227], v[226:227], 0, s[18:19]
	s_mov_b32 m0, s44
	ds_read_b128 v[182:185], v213 offset:49152
	ds_read_b128 v[186:189], v213 offset:50176
	ds_read_b128 v[190:193], v213 offset:51200
	ds_read_b128 v[194:197], v213 offset:52224
	ds_read_b128 v[198:201], v213 offset:53248
	ds_read_b128 v[202:205], v213 offset:54272
	ds_read_b128 v[218:221], v213 offset:55296
	ds_read_b128 v[222:225], v213 offset:56320
	global_load_lds_dwordx4 v[226:227], off
	s_add_i32 m0, s44, 0x2000
	s_add_u32 s42, s42, 0x80080
	v_lshl_add_u64 v[226:227], v[228:229], 0, s[18:19]
	s_addc_u32 s43, s43, 0
	s_add_i32 s44, s85, s66
	global_load_lds_dwordx4 v[226:227], off
	s_mov_b32 m0, s44
	s_nop 0
	global_load_lds_dwordx4 v132, s[42:43]
	s_add_i32 m0, s44, 0x2000
	s_nop 0
	global_load_lds_dwordx4 v136, s[42:43]
	v_lshl_add_u64 v[226:227], v[230:231], 0, s[18:19]
	s_mov_b32 m0, s74
	s_nop 0
	global_load_lds_dwordx4 v[226:227], off
	v_lshl_add_u64 v[226:227], v[232:233], 0, s[18:19]
	s_mov_b32 m0, s75
	s_nop 0
	global_load_lds_dwordx4 v[226:227], off
	s_waitcnt vmcnt(8)
	s_waitcnt lgkmcnt(0)
	s_barrier
	s_setprio 1
	v_mfma_f32_16x16x32_bf16 v[62:65], v[150:153], v[182:185], v[62:65]
	v_mfma_f32_16x16x32_bf16 v[58:61], v[158:161], v[182:185], v[58:61]
	v_mfma_f32_16x16x32_bf16 v[46:49], v[150:153], v[190:193], v[46:49]
	v_mfma_f32_16x16x32_bf16 v[42:45], v[158:161], v[190:193], v[42:45]
	v_mfma_f32_16x16x32_bf16 v[30:33], v[150:153], v[198:201], v[30:33]
	v_mfma_f32_16x16x32_bf16 v[26:29], v[158:161], v[198:201], v[26:29]
	v_mfma_f32_16x16x32_bf16 v[14:17], v[150:153], v[218:221], v[14:17]
	v_mfma_f32_16x16x32_bf16 v[10:13], v[158:161], v[218:221], v[10:13]
	v_mfma_f32_16x16x32_bf16 v[62:65], v[154:157], v[186:189], v[62:65]
	v_mfma_f32_16x16x32_bf16 v[58:61], v[162:165], v[186:189], v[58:61]
	v_mfma_f32_16x16x32_bf16 v[46:49], v[154:157], v[194:197], v[46:49]
	v_mfma_f32_16x16x32_bf16 v[42:45], v[162:165], v[194:197], v[42:45]
	v_mfma_f32_16x16x32_bf16 v[30:33], v[154:157], v[202:205], v[30:33]
	v_mfma_f32_16x16x32_bf16 v[26:29], v[162:165], v[202:205], v[26:29]
	v_mfma_f32_16x16x32_bf16 v[14:17], v[154:157], v[222:225], v[14:17]
	v_mfma_f32_16x16x32_bf16 v[10:13], v[162:165], v[222:225], v[10:13]
	v_mfma_f32_16x16x32_bf16 v[54:57], v[166:169], v[182:185], v[54:57]
	v_mfma_f32_16x16x32_bf16 v[50:53], v[174:177], v[182:185], v[50:53]
	v_mfma_f32_16x16x32_bf16 v[38:41], v[166:169], v[190:193], v[38:41]
	v_mfma_f32_16x16x32_bf16 v[34:37], v[174:177], v[190:193], v[34:37]
	v_mfma_f32_16x16x32_bf16 v[22:25], v[166:169], v[198:201], v[22:25]
	v_mfma_f32_16x16x32_bf16 v[18:21], v[174:177], v[198:201], v[18:21]
	v_mfma_f32_16x16x32_bf16 v[6:9], v[166:169], v[218:221], v[6:9]
	v_mfma_f32_16x16x32_bf16 v[2:5], v[174:177], v[218:221], v[2:5]
	v_mfma_f32_16x16x32_bf16 v[54:57], v[170:173], v[186:189], v[54:57]
	v_mfma_f32_16x16x32_bf16 v[50:53], v[178:181], v[186:189], v[50:53]
	v_mfma_f32_16x16x32_bf16 v[38:41], v[170:173], v[194:197], v[38:41]
	v_mfma_f32_16x16x32_bf16 v[34:37], v[178:181], v[194:197], v[34:37]
	v_mfma_f32_16x16x32_bf16 v[22:25], v[170:173], v[202:205], v[22:25]
	v_mfma_f32_16x16x32_bf16 v[18:21], v[178:181], v[202:205], v[18:21]
	v_mfma_f32_16x16x32_bf16 v[6:9], v[170:173], v[222:225], v[6:9]
	v_mfma_f32_16x16x32_bf16 v[2:5], v[178:181], v[222:225], v[2:5]
	s_setprio 0
	s_barrier
	s_add_i32 s83, s83, 2
	s_add_u32 s36, s36, 0x100
	s_addc_u32 s37, s37, 0
	s_add_u32 s62, s62, 0x100
	s_addc_u32 s63, s63, 0
	s_cmp_gt_u32 s83, 29
	s_cbranch_scc0 .LBB0_466
	s_nop 0
	s_nop 0
	s_nop 0
	s_nop 0
	s_nop 0
	s_nop 0
	s_nop 0
	s_nop 0
	s_nop 0
	s_nop 0
	s_nop 0
	s_nop 0
	s_and_b64 vcc, exec, s[20:21]
	s_cbranch_vccz .LBB0_469
	s_barrier

.LBB0_574:
	ds_read_b128 v[146:149], v152
	ds_read_b128 v[156:159], v152 offset:1024
	ds_read_b128 v[160:163], v152 offset:2048
	ds_read_b128 v[164:167], v152 offset:3072
	ds_read_b128 v[168:171], v153
	ds_read_b128 v[172:175], v153 offset:1024
	ds_read_b128 v[176:179], v153 offset:2048
	ds_read_b128 v[180:183], v153 offset:3072
	s_add_u32 s24, s22, 0xfff80080
	s_addc_u32 s25, s23, -1
	s_cmp_eq_u32 s69, 28
	s_cselect_b32 s27, s15, s25
	s_cselect_b32 s26, s65, s24
	s_cselect_b32 s25, s13, s68
	s_cselect_b32 s24, s66, s67
	s_add_i32 m0, s21, 0xc000
	ds_read_b128 v[184:187], v154
	ds_read_b128 v[188:191], v154 offset:1024
	ds_read_b128 v[192:195], v154 offset:2048
	ds_read_b128 v[196:199], v154 offset:3072
	ds_read_b128 v[200:203], v154 offset:4096
	ds_read_b128 v[204:207], v154 offset:5120
	ds_read_b128 v[208:211], v154 offset:6144
	ds_read_b128 v[212:215], v154 offset:7168
	global_load_lds_dwordx4 v138, s[22:23]
	s_add_i32 m0, s21, 0xe000
	s_nop 0
	global_load_lds_dwordx4 v140, s[22:23]
	s_waitcnt vmcnt(8)
	s_waitcnt lgkmcnt(0)
	s_barrier
	s_setprio 1
	v_mfma_f32_16x16x32_bf16 v[126:129], v[146:149], v[184:187], v[126:129]
	v_mfma_f32_16x16x32_bf16 v[122:125], v[160:163], v[184:187], v[122:125]
	v_mfma_f32_16x16x32_bf16 v[110:113], v[146:149], v[192:195], v[110:113]
	v_mfma_f32_16x16x32_bf16 v[106:109], v[160:163], v[192:195], v[106:109]
	v_mfma_f32_16x16x32_bf16 v[94:97], v[146:149], v[200:203], v[94:97]
	v_mfma_f32_16x16x32_bf16 v[90:93], v[160:163], v[200:203], v[90:93]
	v_mfma_f32_16x16x32_bf16 v[78:81], v[146:149], v[208:211], v[78:81]
	v_mfma_f32_16x16x32_bf16 v[74:77], v[160:163], v[208:211], v[74:77]
	v_mfma_f32_16x16x32_bf16 v[126:129], v[156:159], v[188:191], v[126:129]
	v_mfma_f32_16x16x32_bf16 v[122:125], v[164:167], v[188:191], v[122:125]
	v_mfma_f32_16x16x32_bf16 v[110:113], v[156:159], v[196:199], v[110:113]
	v_mfma_f32_16x16x32_bf16 v[106:109], v[164:167], v[196:199], v[106:109]
	v_mfma_f32_16x16x32_bf16 v[94:97], v[156:159], v[204:207], v[94:97]
	v_mfma_f32_16x16x32_bf16 v[90:93], v[164:167], v[204:207], v[90:93]
	v_mfma_f32_16x16x32_bf16 v[78:81], v[156:159], v[212:215], v[78:81]
	v_mfma_f32_16x16x32_bf16 v[74:77], v[164:167], v[212:215], v[74:77]
	v_mfma_f32_16x16x32_bf16 v[118:121], v[168:171], v[184:187], v[118:121]
	v_mfma_f32_16x16x32_bf16 v[114:117], v[176:179], v[184:187], v[114:117]
	v_mfma_f32_16x16x32_bf16 v[102:105], v[168:171], v[192:195], v[102:105]
	v_mfma_f32_16x16x32_bf16 v[98:101], v[176:179], v[192:195], v[98:101]
	v_mfma_f32_16x16x32_bf16 v[86:89], v[168:171], v[200:203], v[86:89]
	v_mfma_f32_16x16x32_bf16 v[82:85], v[176:179], v[200:203], v[82:85]
	v_mfma_f32_16x16x32_bf16 v[70:73], v[168:171], v[208:211], v[70:73]
	v_mfma_f32_16x16x32_bf16 v[66:69], v[176:179], v[208:211], v[66:69]
	v_mfma_f32_16x16x32_bf16 v[118:121], v[172:175], v[188:191], v[118:121]
	v_mfma_f32_16x16x32_bf16 v[114:117], v[180:183], v[188:191], v[114:117]
	v_mfma_f32_16x16x32_bf16 v[102:105], v[172:175], v[196:199], v[102:105]
	v_mfma_f32_16x16x32_bf16 v[98:101], v[180:183], v[196:199], v[98:101]
	v_mfma_f32_16x16x32_bf16 v[86:89], v[172:175], v[204:207], v[86:89]
	v_mfma_f32_16x16x32_bf16 v[82:85], v[180:183], v[204:207], v[82:85]
	v_mfma_f32_16x16x32_bf16 v[70:73], v[172:175], v[212:215], v[70:73]
	v_mfma_f32_16x16x32_bf16 v[66:69], v[180:183], v[212:215], v[66:69]
	s_setprio 0
	s_barrier
	s_add_i32 s70, s61, s33
	v_lshl_add_u64 v[216:217], s[24:25], 0, v[134:135]
	s_mov_b32 m0, s70
	ds_read_b128 v[184:187], v154 offset:16384
	ds_read_b128 v[188:191], v154 offset:17408
	ds_read_b128 v[192:195], v154 offset:18432
	ds_read_b128 v[196:199], v154 offset:19456
	ds_read_b128 v[200:203], v154 offset:20480
	ds_read_b128 v[204:207], v154 offset:21504
	ds_read_b128 v[208:211], v154 offset:22528
	ds_read_b128 v[212:215], v154 offset:23552
	global_load_lds_dwordx4 v134, s[24:25]
	s_add_i32 m0, s70, 0x2000
	s_add_u32 s70, s24, 0x80000
	v_lshl_add_u64 v[218:219], s[24:25], 0, v[130:131]
	s_addc_u32 s71, s25, 0
	s_add_i32 s72, s62, s33
	global_load_lds_dwordx4 v130, s[24:25]
	s_mov_b32 m0, s72
	v_lshl_add_u64 v[222:223], s[26:27], 0, v[132:133]
	global_load_lds_dwordx4 v134, s[70:71]
	s_add_i32 m0, s72, 0x2000
	s_nop 0
	global_load_lds_dwordx4 v130, s[70:71]
	v_lshl_add_u64 v[220:221], s[26:27], 0, v[136:137]
	s_mov_b32 m0, s21
	s_nop 0
	global_load_lds_dwordx4 v136, s[26:27]
	s_mov_b32 m0, s36
	s_nop 0
	global_load_lds_dwordx4 v132, s[26:27]
	s_waitcnt vmcnt(8)
	s_waitcnt lgkmcnt(0)
	s_barrier
	s_setprio 1
	v_mfma_f32_16x16x32_bf16 v[62:65], v[146:149], v[184:187], v[62:65]
	v_mfma_f32_16x16x32_bf16 v[58:61], v[160:163], v[184:187], v[58:61]
	v_mfma_f32_16x16x32_bf16 v[46:49], v[146:149], v[192:195], v[46:49]
	v_mfma_f32_16x16x32_bf16 v[42:45], v[160:163], v[192:195], v[42:45]
	v_mfma_f32_16x16x32_bf16 v[30:33], v[146:149], v[200:203], v[30:33]
	v_mfma_f32_16x16x32_bf16 v[26:29], v[160:163], v[200:203], v[26:29]
	v_mfma_f32_16x16x32_bf16 v[14:17], v[146:149], v[208:211], v[14:17]
	v_mfma_f32_16x16x32_bf16 v[10:13], v[160:163], v[208:211], v[10:13]
	v_mfma_f32_16x16x32_bf16 v[62:65], v[156:159], v[188:191], v[62:65]
	v_mfma_f32_16x16x32_bf16 v[58:61], v[164:167], v[188:191], v[58:61]
	v_mfma_f32_16x16x32_bf16 v[46:49], v[156:159], v[196:199], v[46:49]
	v_mfma_f32_16x16x32_bf16 v[42:45], v[164:167], v[196:199], v[42:45]
	v_mfma_f32_16x16x32_bf16 v[30:33], v[156:159], v[204:207], v[30:33]
	v_mfma_f32_16x16x32_bf16 v[26:29], v[164:167], v[204:207], v[26:29]
	v_mfma_f32_16x16x32_bf16 v[14:17], v[156:159], v[212:215], v[14:17]
	v_mfma_f32_16x16x32_bf16 v[10:13], v[164:167], v[212:215], v[10:13]
	v_mfma_f32_16x16x32_bf16 v[54:57], v[168:171], v[184:187], v[54:57]
	v_mfma_f32_16x16x32_bf16 v[50:53], v[176:179], v[184:187], v[50:53]
	v_mfma_f32_16x16x32_bf16 v[38:41], v[168:171], v[192:195], v[38:41]
	v_mfma_f32_16x16x32_bf16 v[34:37], v[176:179], v[192:195], v[34:37]
	v_mfma_f32_16x16x32_bf16 v[22:25], v[168:171], v[200:203], v[22:25]
	v_mfma_f32_16x16x32_bf16 v[18:21], v[176:179], v[200:203], v[18:21]
	v_mfma_f32_16x16x32_bf16 v[6:9], v[168:171], v[208:211], v[6:9]
	v_mfma_f32_16x16x32_bf16 v[2:5], v[176:179], v[208:211], v[2:5]
	v_mfma_f32_16x16x32_bf16 v[54:57], v[172:175], v[188:191], v[54:57]
	v_mfma_f32_16x16x32_bf16 v[50:53], v[180:183], v[188:191], v[50:53]
	v_mfma_f32_16x16x32_bf16 v[38:41], v[172:175], v[196:199], v[38:41]
	v_mfma_f32_16x16x32_bf16 v[34:37], v[180:183], v[196:199], v[34:37]
	v_mfma_f32_16x16x32_bf16 v[22:25], v[172:175], v[204:207], v[22:25]
	v_mfma_f32_16x16x32_bf16 v[18:21], v[180:183], v[204:207], v[18:21]
	v_mfma_f32_16x16x32_bf16 v[6:9], v[172:175], v[212:215], v[6:9]
	v_mfma_f32_16x16x32_bf16 v[2:5], v[180:183], v[212:215], v[2:5]
	s_setprio 0
	s_barrier
	s_add_i32 s70, 0, 0x18000
	v_add_u32_e32 v155, s70, v150
	s_add_i32 s71, 0, 0x1c000
	ds_read_b128 v[146:149], v155
	ds_read_b128 v[156:159], v155 offset:1024
	ds_read_b128 v[160:163], v155 offset:2048
	ds_read_b128 v[164:167], v155 offset:3072
	v_add_u32_e32 v155, s71, v150
	ds_read_b128 v[168:171], v155
	ds_read_b128 v[172:175], v155 offset:1024
	ds_read_b128 v[176:179], v155 offset:2048
	ds_read_b128 v[180:183], v155 offset:3072
	s_add_u32 s26, s26, 0x80000
	s_addc_u32 s27, s27, 0
	s_mov_b32 m0, s37
	ds_read_b128 v[184:187], v154 offset:32768
	ds_read_b128 v[188:191], v154 offset:33792
	ds_read_b128 v[192:195], v154 offset:34816
	ds_read_b128 v[196:199], v154 offset:35840
	ds_read_b128 v[200:203], v154 offset:36864
	ds_read_b128 v[204:207], v154 offset:37888
	ds_read_b128 v[208:211], v154 offset:38912
	ds_read_b128 v[212:215], v154 offset:39936
	global_load_lds_dwordx4 v136, s[26:27]
	s_mov_b32 m0, s42
	s_nop 0
	global_load_lds_dwordx4 v132, s[26:27]
	s_waitcnt vmcnt(8)
	s_waitcnt lgkmcnt(0)
	s_barrier
	s_setprio 1
	v_mfma_f32_16x16x32_bf16 v[126:129], v[146:149], v[184:187], v[126:129]
	v_mfma_f32_16x16x32_bf16 v[122:125], v[160:163], v[184:187], v[122:125]
	v_mfma_f32_16x16x32_bf16 v[110:113], v[146:149], v[192:195], v[110:113]
	v_mfma_f32_16x16x32_bf16 v[106:109], v[160:163], v[192:195], v[106:109]
	v_mfma_f32_16x16x32_bf16 v[94:97], v[146:149], v[200:203], v[94:97]
	v_mfma_f32_16x16x32_bf16 v[90:93], v[160:163], v[200:203], v[90:93]
	v_mfma_f32_16x16x32_bf16 v[78:81], v[146:149], v[208:211], v[78:81]
	v_mfma_f32_16x16x32_bf16 v[74:77], v[160:163], v[208:211], v[74:77]
	v_mfma_f32_16x16x32_bf16 v[126:129], v[156:159], v[188:191], v[126:129]
	v_mfma_f32_16x16x32_bf16 v[122:125], v[164:167], v[188:191], v[122:125]
	v_mfma_f32_16x16x32_bf16 v[110:113], v[156:159], v[196:199], v[110:113]
	v_mfma_f32_16x16x32_bf16 v[106:109], v[164:167], v[196:199], v[106:109]
	v_mfma_f32_16x16x32_bf16 v[94:97], v[156:159], v[204:207], v[94:97]
	v_mfma_f32_16x16x32_bf16 v[90:93], v[164:167], v[204:207], v[90:93]
	v_mfma_f32_16x16x32_bf16 v[78:81], v[156:159], v[212:215], v[78:81]
	v_mfma_f32_16x16x32_bf16 v[74:77], v[164:167], v[212:215], v[74:77]
	v_mfma_f32_16x16x32_bf16 v[118:121], v[168:171], v[184:187], v[118:121]
	v_mfma_f32_16x16x32_bf16 v[114:117], v[176:179], v[184:187], v[114:117]
	v_mfma_f32_16x16x32_bf16 v[102:105], v[168:171], v[192:195], v[102:105]
	v_mfma_f32_16x16x32_bf16 v[98:101], v[176:179], v[192:195], v[98:101]
	v_mfma_f32_16x16x32_bf16 v[86:89], v[168:171], v[200:203], v[86:89]
	v_mfma_f32_16x16x32_bf16 v[82:85], v[176:179], v[200:203], v[82:85]
	v_mfma_f32_16x16x32_bf16 v[70:73], v[168:171], v[208:211], v[70:73]
	v_mfma_f32_16x16x32_bf16 v[66:69], v[176:179], v[208:211], v[66:69]
	v_mfma_f32_16x16x32_bf16 v[118:121], v[172:175], v[188:191], v[118:121]
	v_mfma_f32_16x16x32_bf16 v[114:117], v[180:183], v[188:191], v[114:117]
	v_mfma_f32_16x16x32_bf16 v[102:105], v[172:175], v[196:199], v[102:105]
	v_mfma_f32_16x16x32_bf16 v[98:101], v[180:183], v[196:199], v[98:101]
	v_mfma_f32_16x16x32_bf16 v[86:89], v[172:175], v[204:207], v[86:89]
	v_mfma_f32_16x16x32_bf16 v[82:85], v[180:183], v[204:207], v[82:85]
	v_mfma_f32_16x16x32_bf16 v[70:73], v[172:175], v[212:215], v[70:73]
	v_mfma_f32_16x16x32_bf16 v[66:69], v[180:183], v[212:215], v[66:69]
	s_setprio 0
	s_barrier
	s_add_i32 s26, s70, s33
	v_lshl_add_u64 v[216:217], v[216:217], 0, s[8:9]
	s_mov_b32 m0, s26
	ds_read_b128 v[184:187], v154 offset:49152
	ds_read_b128 v[188:191], v154 offset:50176
	ds_read_b128 v[192:195], v154 offset:51200
	ds_read_b128 v[196:199], v154 offset:52224
	ds_read_b128 v[200:203], v154 offset:53248
	ds_read_b128 v[204:207], v154 offset:54272
	ds_read_b128 v[208:211], v154 offset:55296
	ds_read_b128 v[212:215], v154 offset:56320
	global_load_lds_dwordx4 v[216:217], off
	s_add_i32 m0, s26, 0x2000
	s_add_u32 s24, s24, 0x80080
	v_lshl_add_u64 v[216:217], v[218:219], 0, s[8:9]
	s_addc_u32 s25, s25, 0
	s_add_i32 s26, s71, s33
	global_load_lds_dwordx4 v[216:217], off
	s_mov_b32 m0, s26
	s_nop 0
	global_load_lds_dwordx4 v134, s[24:25]
	s_add_i32 m0, s26, 0x2000
	s_nop 0
	global_load_lds_dwordx4 v130, s[24:25]
	v_lshl_add_u64 v[216:217], v[220:221], 0, s[8:9]
	s_mov_b32 m0, s44
	s_nop 0
	global_load_lds_dwordx4 v[216:217], off
	v_lshl_add_u64 v[216:217], v[222:223], 0, s[8:9]
	s_mov_b32 m0, s45
	s_nop 0
	global_load_lds_dwordx4 v[216:217], off
	s_waitcnt vmcnt(8)
	s_waitcnt lgkmcnt(0)
	s_barrier
	s_setprio 1
	v_mfma_f32_16x16x32_bf16 v[62:65], v[146:149], v[184:187], v[62:65]
	v_mfma_f32_16x16x32_bf16 v[58:61], v[160:163], v[184:187], v[58:61]
	v_mfma_f32_16x16x32_bf16 v[46:49], v[146:149], v[192:195], v[46:49]
	v_mfma_f32_16x16x32_bf16 v[42:45], v[160:163], v[192:195], v[42:45]
	v_mfma_f32_16x16x32_bf16 v[30:33], v[146:149], v[200:203], v[30:33]
	v_mfma_f32_16x16x32_bf16 v[26:29], v[160:163], v[200:203], v[26:29]
	v_mfma_f32_16x16x32_bf16 v[14:17], v[146:149], v[208:211], v[14:17]
	v_mfma_f32_16x16x32_bf16 v[10:13], v[160:163], v[208:211], v[10:13]
	v_mfma_f32_16x16x32_bf16 v[62:65], v[156:159], v[188:191], v[62:65]
	v_mfma_f32_16x16x32_bf16 v[58:61], v[164:167], v[188:191], v[58:61]
	v_mfma_f32_16x16x32_bf16 v[46:49], v[156:159], v[196:199], v[46:49]
	v_mfma_f32_16x16x32_bf16 v[42:45], v[164:167], v[196:199], v[42:45]
	v_mfma_f32_16x16x32_bf16 v[30:33], v[156:159], v[204:207], v[30:33]
	v_mfma_f32_16x16x32_bf16 v[26:29], v[164:167], v[204:207], v[26:29]
	v_mfma_f32_16x16x32_bf16 v[14:17], v[156:159], v[212:215], v[14:17]
	v_mfma_f32_16x16x32_bf16 v[10:13], v[164:167], v[212:215], v[10:13]
	v_mfma_f32_16x16x32_bf16 v[54:57], v[168:171], v[184:187], v[54:57]
	v_mfma_f32_16x16x32_bf16 v[50:53], v[176:179], v[184:187], v[50:53]
	v_mfma_f32_16x16x32_bf16 v[38:41], v[168:171], v[192:195], v[38:41]
	v_mfma_f32_16x16x32_bf16 v[34:37], v[176:179], v[192:195], v[34:37]
	v_mfma_f32_16x16x32_bf16 v[22:25], v[168:171], v[200:203], v[22:25]
	v_mfma_f32_16x16x32_bf16 v[18:21], v[176:179], v[200:203], v[18:21]
	v_mfma_f32_16x16x32_bf16 v[6:9], v[168:171], v[208:211], v[6:9]
	v_mfma_f32_16x16x32_bf16 v[2:5], v[176:179], v[208:211], v[2:5]
	v_mfma_f32_16x16x32_bf16 v[54:57], v[172:175], v[188:191], v[54:57]
	v_mfma_f32_16x16x32_bf16 v[50:53], v[180:183], v[188:191], v[50:53]
	v_mfma_f32_16x16x32_bf16 v[38:41], v[172:175], v[196:199], v[38:41]
	v_mfma_f32_16x16x32_bf16 v[34:37], v[180:183], v[196:199], v[34:37]
	v_mfma_f32_16x16x32_bf16 v[22:25], v[172:175], v[204:207], v[22:25]
	v_mfma_f32_16x16x32_bf16 v[18:21], v[180:183], v[204:207], v[18:21]
	v_mfma_f32_16x16x32_bf16 v[6:9], v[172:175], v[212:215], v[6:9]
	v_mfma_f32_16x16x32_bf16 v[2:5], v[180:183], v[212:215], v[2:5]
	s_setprio 0
	s_barrier
	s_add_i32 s69, s69, 2
	s_add_u32 s22, s22, 0x100
	s_addc_u32 s23, s23, 0
	s_add_u32 s67, s67, 0x100
	s_addc_u32 s68, s68, 0
	s_cmp_gt_u32 s69, 29
	s_cbranch_scc0 .LBB0_574
	s_nop 0
	s_nop 0
	s_nop 0
	s_nop 0
	s_nop 0
	s_nop 0
	s_nop 0
	s_nop 0
	s_nop 0
	s_nop 0
	s_nop 0
	s_nop 0
	s_and_b64 vcc, exec, s[10:11]
	s_cbranch_vccz .LBB0_577
	s_barrier

.LBB0_659:
	ds_read_b128 v[150:153], v211
	ds_read_b128 v[154:157], v211 offset:1024
	ds_read_b128 v[158:161], v211 offset:2048
	ds_read_b128 v[162:165], v211 offset:3072
	ds_read_b128 v[166:169], v212
	ds_read_b128 v[170:173], v212 offset:1024
	ds_read_b128 v[174:177], v212 offset:2048
	ds_read_b128 v[178:181], v212 offset:3072
	s_add_u32 s36, s0, 0xffea8080
	s_addc_u32 s37, s1, -1
	s_cmpk_eq_i32 s44, 0x52
	s_cselect_b32 s43, s27, s37
	s_cselect_b32 s42, s26, s36
	s_cselect_b32 s37, s29, s35
	s_cselect_b32 s36, s28, s31
	s_add_i32 m0, s63, 0xc000
	ds_read_b128 v[182:185], v213
	ds_read_b128 v[186:189], v213 offset:1024
	ds_read_b128 v[190:193], v213 offset:2048
	ds_read_b128 v[194:197], v213 offset:3072
	ds_read_b128 v[198:201], v213 offset:4096
	ds_read_b128 v[202:205], v213 offset:5120
	ds_read_b128 v[218:221], v213 offset:6144
	ds_read_b128 v[222:225], v213 offset:7168
	global_load_lds_dwordx4 v142, s[0:1]
	s_add_i32 m0, s63, 0xe000
	s_nop 0
	global_load_lds_dwordx4 v144, s[0:1]
	s_waitcnt vmcnt(8)
	s_waitcnt lgkmcnt(0)
	s_barrier
	s_setprio 1
	v_mfma_f32_16x16x32_bf16 v[126:129], v[150:153], v[182:185], v[126:129]
	v_mfma_f32_16x16x32_bf16 v[122:125], v[158:161], v[182:185], v[122:125]
	v_mfma_f32_16x16x32_bf16 v[110:113], v[150:153], v[190:193], v[110:113]
	v_mfma_f32_16x16x32_bf16 v[106:109], v[158:161], v[190:193], v[106:109]
	v_mfma_f32_16x16x32_bf16 v[94:97], v[150:153], v[198:201], v[94:97]
	v_mfma_f32_16x16x32_bf16 v[90:93], v[158:161], v[198:201], v[90:93]
	v_mfma_f32_16x16x32_bf16 v[78:81], v[150:153], v[218:221], v[78:81]
	v_mfma_f32_16x16x32_bf16 v[74:77], v[158:161], v[218:221], v[74:77]
	v_mfma_f32_16x16x32_bf16 v[126:129], v[154:157], v[186:189], v[126:129]
	v_mfma_f32_16x16x32_bf16 v[122:125], v[162:165], v[186:189], v[122:125]
	v_mfma_f32_16x16x32_bf16 v[110:113], v[154:157], v[194:197], v[110:113]
	v_mfma_f32_16x16x32_bf16 v[106:109], v[162:165], v[194:197], v[106:109]
	v_mfma_f32_16x16x32_bf16 v[94:97], v[154:157], v[202:205], v[94:97]
	v_mfma_f32_16x16x32_bf16 v[90:93], v[162:165], v[202:205], v[90:93]
	v_mfma_f32_16x16x32_bf16 v[78:81], v[154:157], v[222:225], v[78:81]
	v_mfma_f32_16x16x32_bf16 v[74:77], v[162:165], v[222:225], v[74:77]
	v_mfma_f32_16x16x32_bf16 v[118:121], v[166:169], v[182:185], v[118:121]
	v_mfma_f32_16x16x32_bf16 v[114:117], v[174:177], v[182:185], v[114:117]
	v_mfma_f32_16x16x32_bf16 v[102:105], v[166:169], v[190:193], v[102:105]
	v_mfma_f32_16x16x32_bf16 v[98:101], v[174:177], v[190:193], v[98:101]
	v_mfma_f32_16x16x32_bf16 v[86:89], v[166:169], v[198:201], v[86:89]
	v_mfma_f32_16x16x32_bf16 v[82:85], v[174:177], v[198:201], v[82:85]
	v_mfma_f32_16x16x32_bf16 v[70:73], v[166:169], v[218:221], v[70:73]
	v_mfma_f32_16x16x32_bf16 v[66:69], v[174:177], v[218:221], v[66:69]
	v_mfma_f32_16x16x32_bf16 v[118:121], v[170:173], v[186:189], v[118:121]
	v_mfma_f32_16x16x32_bf16 v[114:117], v[178:181], v[186:189], v[114:117]
	v_mfma_f32_16x16x32_bf16 v[102:105], v[170:173], v[194:197], v[102:105]
	v_mfma_f32_16x16x32_bf16 v[98:101], v[178:181], v[194:197], v[98:101]
	v_mfma_f32_16x16x32_bf16 v[86:89], v[170:173], v[202:205], v[86:89]
	v_mfma_f32_16x16x32_bf16 v[82:85], v[178:181], v[202:205], v[82:85]
	v_mfma_f32_16x16x32_bf16 v[70:73], v[170:173], v[222:225], v[70:73]
	v_mfma_f32_16x16x32_bf16 v[66:69], v[178:181], v[222:225], v[66:69]
	s_setprio 0
	s_barrier
	s_add_i32 s45, s75, s62
	v_lshl_add_u64 v[226:227], s[36:37], 0, v[132:133]
	s_mov_b32 m0, s45
	ds_read_b128 v[182:185], v213 offset:16384
	ds_read_b128 v[186:189], v213 offset:17408
	ds_read_b128 v[190:193], v213 offset:18432
	ds_read_b128 v[194:197], v213 offset:19456
	ds_read_b128 v[198:201], v213 offset:20480
	ds_read_b128 v[202:205], v213 offset:21504
	ds_read_b128 v[218:221], v213 offset:22528
	ds_read_b128 v[222:225], v213 offset:23552
	global_load_lds_dwordx4 v132, s[36:37]
	s_add_i32 m0, s45, 0x2000
	s_add_u32 s82, s36, 0x158000
	v_lshl_add_u64 v[228:229], s[36:37], 0, v[136:137]
	s_addc_u32 s83, s37, 0
	s_add_i32 s45, s76, s62
	global_load_lds_dwordx4 v136, s[36:37]
	s_mov_b32 m0, s45
	v_lshl_add_u64 v[232:233], s[42:43], 0, v[134:135]
	global_load_lds_dwordx4 v132, s[82:83]
	s_add_i32 m0, s45, 0x2000
	s_nop 0
	global_load_lds_dwordx4 v136, s[82:83]
	v_lshl_add_u64 v[230:231], s[42:43], 0, v[130:131]
	s_mov_b32 m0, s63
	s_nop 0
	global_load_lds_dwordx4 v130, s[42:43]
	s_mov_b32 m0, s64
	s_nop 0
	global_load_lds_dwordx4 v134, s[42:43]
	s_waitcnt vmcnt(8)
	s_waitcnt lgkmcnt(0)
	s_barrier
	s_setprio 1
	v_mfma_f32_16x16x32_bf16 v[62:65], v[150:153], v[182:185], v[62:65]
	v_mfma_f32_16x16x32_bf16 v[58:61], v[158:161], v[182:185], v[58:61]
	v_mfma_f32_16x16x32_bf16 v[46:49], v[150:153], v[190:193], v[46:49]
	v_mfma_f32_16x16x32_bf16 v[42:45], v[158:161], v[190:193], v[42:45]
	v_mfma_f32_16x16x32_bf16 v[30:33], v[150:153], v[198:201], v[30:33]
	v_mfma_f32_16x16x32_bf16 v[26:29], v[158:161], v[198:201], v[26:29]
	v_mfma_f32_16x16x32_bf16 v[14:17], v[150:153], v[218:221], v[14:17]
	v_mfma_f32_16x16x32_bf16 v[10:13], v[158:161], v[218:221], v[10:13]
	v_mfma_f32_16x16x32_bf16 v[62:65], v[154:157], v[186:189], v[62:65]
	v_mfma_f32_16x16x32_bf16 v[58:61], v[162:165], v[186:189], v[58:61]
	v_mfma_f32_16x16x32_bf16 v[46:49], v[154:157], v[194:197], v[46:49]
	v_mfma_f32_16x16x32_bf16 v[42:45], v[162:165], v[194:197], v[42:45]
	v_mfma_f32_16x16x32_bf16 v[30:33], v[154:157], v[202:205], v[30:33]
	v_mfma_f32_16x16x32_bf16 v[26:29], v[162:165], v[202:205], v[26:29]
	v_mfma_f32_16x16x32_bf16 v[14:17], v[154:157], v[222:225], v[14:17]
	v_mfma_f32_16x16x32_bf16 v[10:13], v[162:165], v[222:225], v[10:13]
	v_mfma_f32_16x16x32_bf16 v[54:57], v[166:169], v[182:185], v[54:57]
	v_mfma_f32_16x16x32_bf16 v[50:53], v[174:177], v[182:185], v[50:53]
	v_mfma_f32_16x16x32_bf16 v[38:41], v[166:169], v[190:193], v[38:41]
	v_mfma_f32_16x16x32_bf16 v[34:37], v[174:177], v[190:193], v[34:37]
	v_mfma_f32_16x16x32_bf16 v[22:25], v[166:169], v[198:201], v[22:25]
	v_mfma_f32_16x16x32_bf16 v[18:21], v[174:177], v[198:201], v[18:21]
	v_mfma_f32_16x16x32_bf16 v[6:9], v[166:169], v[218:221], v[6:9]
	v_mfma_f32_16x16x32_bf16 v[2:5], v[174:177], v[218:221], v[2:5]
	v_mfma_f32_16x16x32_bf16 v[54:57], v[170:173], v[186:189], v[54:57]
	v_mfma_f32_16x16x32_bf16 v[50:53], v[178:181], v[186:189], v[50:53]
	v_mfma_f32_16x16x32_bf16 v[38:41], v[170:173], v[194:197], v[38:41]
	v_mfma_f32_16x16x32_bf16 v[34:37], v[178:181], v[194:197], v[34:37]
	v_mfma_f32_16x16x32_bf16 v[22:25], v[170:173], v[202:205], v[22:25]
	v_mfma_f32_16x16x32_bf16 v[18:21], v[178:181], v[202:205], v[18:21]
	v_mfma_f32_16x16x32_bf16 v[6:9], v[170:173], v[222:225], v[6:9]
	v_mfma_f32_16x16x32_bf16 v[2:5], v[178:181], v[222:225], v[2:5]
	s_setprio 0
	s_barrier
	s_add_i32 s45, 0, 0x18000
	v_add_u32_e32 v139, s45, v206
	s_add_i32 s81, 0, 0x1c000
	ds_read_b128 v[150:153], v139
	ds_read_b128 v[154:157], v139 offset:1024
	ds_read_b128 v[158:161], v139 offset:2048
	ds_read_b128 v[162:165], v139 offset:3072
	v_add_u32_e32 v139, s81, v206
	ds_read_b128 v[166:169], v139
	ds_read_b128 v[170:173], v139 offset:1024
	ds_read_b128 v[174:177], v139 offset:2048
	ds_read_b128 v[178:181], v139 offset:3072
	s_add_u32 s42, s42, 0x158000
	s_addc_u32 s43, s43, 0
	s_mov_b32 m0, s65
	ds_read_b128 v[182:185], v213 offset:32768
	ds_read_b128 v[186:189], v213 offset:33792
	ds_read_b128 v[190:193], v213 offset:34816
	ds_read_b128 v[194:197], v213 offset:35840
	ds_read_b128 v[198:201], v213 offset:36864
	ds_read_b128 v[202:205], v213 offset:37888
	ds_read_b128 v[218:221], v213 offset:38912
	ds_read_b128 v[222:225], v213 offset:39936
	global_load_lds_dwordx4 v130, s[42:43]
	s_mov_b32 m0, s66
	s_nop 0
	global_load_lds_dwordx4 v134, s[42:43]
	s_waitcnt vmcnt(8)
	s_waitcnt lgkmcnt(0)
	s_barrier
	s_setprio 1
	v_mfma_f32_16x16x32_bf16 v[126:129], v[150:153], v[182:185], v[126:129]
	v_mfma_f32_16x16x32_bf16 v[122:125], v[158:161], v[182:185], v[122:125]
	v_mfma_f32_16x16x32_bf16 v[110:113], v[150:153], v[190:193], v[110:113]
	v_mfma_f32_16x16x32_bf16 v[106:109], v[158:161], v[190:193], v[106:109]
	v_mfma_f32_16x16x32_bf16 v[94:97], v[150:153], v[198:201], v[94:97]
	v_mfma_f32_16x16x32_bf16 v[90:93], v[158:161], v[198:201], v[90:93]
	v_mfma_f32_16x16x32_bf16 v[78:81], v[150:153], v[218:221], v[78:81]
	v_mfma_f32_16x16x32_bf16 v[74:77], v[158:161], v[218:221], v[74:77]
	v_mfma_f32_16x16x32_bf16 v[126:129], v[154:157], v[186:189], v[126:129]
	v_mfma_f32_16x16x32_bf16 v[122:125], v[162:165], v[186:189], v[122:125]
	v_mfma_f32_16x16x32_bf16 v[110:113], v[154:157], v[194:197], v[110:113]
	v_mfma_f32_16x16x32_bf16 v[106:109], v[162:165], v[194:197], v[106:109]
	v_mfma_f32_16x16x32_bf16 v[94:97], v[154:157], v[202:205], v[94:97]
	v_mfma_f32_16x16x32_bf16 v[90:93], v[162:165], v[202:205], v[90:93]
	v_mfma_f32_16x16x32_bf16 v[78:81], v[154:157], v[222:225], v[78:81]
	v_mfma_f32_16x16x32_bf16 v[74:77], v[162:165], v[222:225], v[74:77]
	v_mfma_f32_16x16x32_bf16 v[118:121], v[166:169], v[182:185], v[118:121]
	v_mfma_f32_16x16x32_bf16 v[114:117], v[174:177], v[182:185], v[114:117]
	v_mfma_f32_16x16x32_bf16 v[102:105], v[166:169], v[190:193], v[102:105]
	v_mfma_f32_16x16x32_bf16 v[98:101], v[174:177], v[190:193], v[98:101]
	v_mfma_f32_16x16x32_bf16 v[86:89], v[166:169], v[198:201], v[86:89]
	v_mfma_f32_16x16x32_bf16 v[82:85], v[174:177], v[198:201], v[82:85]
	v_mfma_f32_16x16x32_bf16 v[70:73], v[166:169], v[218:221], v[70:73]
	v_mfma_f32_16x16x32_bf16 v[66:69], v[174:177], v[218:221], v[66:69]
	v_mfma_f32_16x16x32_bf16 v[118:121], v[170:173], v[186:189], v[118:121]
	v_mfma_f32_16x16x32_bf16 v[114:117], v[178:181], v[186:189], v[114:117]
	v_mfma_f32_16x16x32_bf16 v[102:105], v[170:173], v[194:197], v[102:105]
	v_mfma_f32_16x16x32_bf16 v[98:101], v[178:181], v[194:197], v[98:101]
	v_mfma_f32_16x16x32_bf16 v[86:89], v[170:173], v[202:205], v[86:89]
	v_mfma_f32_16x16x32_bf16 v[82:85], v[178:181], v[202:205], v[82:85]
	v_mfma_f32_16x16x32_bf16 v[70:73], v[170:173], v[222:225], v[70:73]
	v_mfma_f32_16x16x32_bf16 v[66:69], v[178:181], v[222:225], v[66:69]
	s_setprio 0
	s_barrier
	s_add_i32 s42, s45, s62
	v_lshl_add_u64 v[226:227], v[226:227], 0, s[20:21]
	s_mov_b32 m0, s42
	ds_read_b128 v[182:185], v213 offset:49152
	ds_read_b128 v[186:189], v213 offset:50176
	ds_read_b128 v[190:193], v213 offset:51200
	ds_read_b128 v[194:197], v213 offset:52224
	ds_read_b128 v[198:201], v213 offset:53248
	ds_read_b128 v[202:205], v213 offset:54272
	ds_read_b128 v[218:221], v213 offset:55296
	ds_read_b128 v[222:225], v213 offset:56320
	global_load_lds_dwordx4 v[226:227], off
	s_add_i32 m0, s42, 0x2000
	s_add_u32 s36, s36, 0x158080
	v_lshl_add_u64 v[226:227], v[228:229], 0, s[20:21]
	s_addc_u32 s37, s37, 0
	s_add_i32 s42, s81, s62
	global_load_lds_dwordx4 v[226:227], off
	s_mov_b32 m0, s42
	s_nop 0
	global_load_lds_dwordx4 v132, s[36:37]
	s_add_i32 m0, s42, 0x2000
	s_nop 0
	global_load_lds_dwordx4 v136, s[36:37]
	v_lshl_add_u64 v[226:227], v[230:231], 0, s[20:21]
	s_mov_b32 m0, s70
	s_nop 0
	global_load_lds_dwordx4 v[226:227], off
	v_lshl_add_u64 v[226:227], v[232:233], 0, s[20:21]
	s_mov_b32 m0, s71
	s_nop 0
	global_load_lds_dwordx4 v[226:227], off
	s_waitcnt vmcnt(8)
	s_waitcnt lgkmcnt(0)
	s_barrier
	s_setprio 1
	v_mfma_f32_16x16x32_bf16 v[62:65], v[150:153], v[182:185], v[62:65]
	v_mfma_f32_16x16x32_bf16 v[58:61], v[158:161], v[182:185], v[58:61]
	v_mfma_f32_16x16x32_bf16 v[46:49], v[150:153], v[190:193], v[46:49]
	v_mfma_f32_16x16x32_bf16 v[42:45], v[158:161], v[190:193], v[42:45]
	v_mfma_f32_16x16x32_bf16 v[30:33], v[150:153], v[198:201], v[30:33]
	v_mfma_f32_16x16x32_bf16 v[26:29], v[158:161], v[198:201], v[26:29]
	v_mfma_f32_16x16x32_bf16 v[14:17], v[150:153], v[218:221], v[14:17]
	v_mfma_f32_16x16x32_bf16 v[10:13], v[158:161], v[218:221], v[10:13]
	v_mfma_f32_16x16x32_bf16 v[62:65], v[154:157], v[186:189], v[62:65]
	v_mfma_f32_16x16x32_bf16 v[58:61], v[162:165], v[186:189], v[58:61]
	v_mfma_f32_16x16x32_bf16 v[46:49], v[154:157], v[194:197], v[46:49]
	v_mfma_f32_16x16x32_bf16 v[42:45], v[162:165], v[194:197], v[42:45]
	v_mfma_f32_16x16x32_bf16 v[30:33], v[154:157], v[202:205], v[30:33]
	v_mfma_f32_16x16x32_bf16 v[26:29], v[162:165], v[202:205], v[26:29]
	v_mfma_f32_16x16x32_bf16 v[14:17], v[154:157], v[222:225], v[14:17]
	v_mfma_f32_16x16x32_bf16 v[10:13], v[162:165], v[222:225], v[10:13]
	v_mfma_f32_16x16x32_bf16 v[54:57], v[166:169], v[182:185], v[54:57]
	v_mfma_f32_16x16x32_bf16 v[50:53], v[174:177], v[182:185], v[50:53]
	v_mfma_f32_16x16x32_bf16 v[38:41], v[166:169], v[190:193], v[38:41]
	v_mfma_f32_16x16x32_bf16 v[34:37], v[174:177], v[190:193], v[34:37]
	v_mfma_f32_16x16x32_bf16 v[22:25], v[166:169], v[198:201], v[22:25]
	v_mfma_f32_16x16x32_bf16 v[18:21], v[174:177], v[198:201], v[18:21]
	v_mfma_f32_16x16x32_bf16 v[6:9], v[166:169], v[218:221], v[6:9]
	v_mfma_f32_16x16x32_bf16 v[2:5], v[174:177], v[218:221], v[2:5]
	v_mfma_f32_16x16x32_bf16 v[54:57], v[170:173], v[186:189], v[54:57]
	v_mfma_f32_16x16x32_bf16 v[50:53], v[178:181], v[186:189], v[50:53]
	v_mfma_f32_16x16x32_bf16 v[38:41], v[170:173], v[194:197], v[38:41]
	v_mfma_f32_16x16x32_bf16 v[34:37], v[178:181], v[194:197], v[34:37]
	v_mfma_f32_16x16x32_bf16 v[22:25], v[170:173], v[202:205], v[22:25]
	v_mfma_f32_16x16x32_bf16 v[18:21], v[178:181], v[202:205], v[18:21]
	v_mfma_f32_16x16x32_bf16 v[6:9], v[170:173], v[222:225], v[6:9]
	v_mfma_f32_16x16x32_bf16 v[2:5], v[178:181], v[222:225], v[2:5]
	s_setprio 0
	s_barrier
	s_add_i32 s44, s44, 2
	s_add_u32 s0, s0, 0x100
	s_addc_u32 s1, s1, 0
	s_add_u32 s31, s31, 0x100
	s_addc_u32 s35, s35, 0
	s_cmpk_gt_u32 s44, 0x53
	s_cbranch_scc0 .LBB0_659
	s_nop 0
	s_nop 0
	s_nop 0
	s_nop 0
	s_nop 0
	s_nop 0
	s_nop 0
	s_nop 0
	s_nop 0
	s_nop 0
	s_nop 0
	s_nop 0
	s_and_b64 vcc, exec, s[22:23]
	s_cbranch_vccz .LBB0_662
	s_barrier

.LBB0_767:
	ds_read_b128 v[146:149], v152
	ds_read_b128 v[156:159], v152 offset:1024
	ds_read_b128 v[160:163], v152 offset:2048
	ds_read_b128 v[164:167], v152 offset:3072
	ds_read_b128 v[168:171], v153
	ds_read_b128 v[172:175], v153 offset:1024
	ds_read_b128 v[176:179], v153 offset:2048
	ds_read_b128 v[180:183], v153 offset:3072
	s_add_u32 s24, s22, 0xfff80080
	s_addc_u32 s25, s23, -1
	s_cmp_eq_u32 s69, 28
	s_cselect_b32 s27, s15, s25
	s_cselect_b32 s26, s65, s24
	s_cselect_b32 s25, s13, s68
	s_cselect_b32 s24, s66, s67
	s_add_i32 m0, s21, 0xc000
	ds_read_b128 v[184:187], v154
	ds_read_b128 v[188:191], v154 offset:1024
	ds_read_b128 v[192:195], v154 offset:2048
	ds_read_b128 v[196:199], v154 offset:3072
	ds_read_b128 v[200:203], v154 offset:4096
	ds_read_b128 v[204:207], v154 offset:5120
	ds_read_b128 v[208:211], v154 offset:6144
	ds_read_b128 v[212:215], v154 offset:7168
	global_load_lds_dwordx4 v138, s[22:23]
	s_add_i32 m0, s21, 0xe000
	s_nop 0
	global_load_lds_dwordx4 v140, s[22:23]
	s_waitcnt vmcnt(8)
	s_waitcnt lgkmcnt(0)
	s_barrier
	s_setprio 1
	v_mfma_f32_16x16x32_bf16 v[126:129], v[146:149], v[184:187], v[126:129]
	v_mfma_f32_16x16x32_bf16 v[122:125], v[160:163], v[184:187], v[122:125]
	v_mfma_f32_16x16x32_bf16 v[118:121], v[146:149], v[192:195], v[118:121]
	v_mfma_f32_16x16x32_bf16 v[110:113], v[160:163], v[192:195], v[110:113]
	v_mfma_f32_16x16x32_bf16 v[102:105], v[146:149], v[200:203], v[102:105]
	v_mfma_f32_16x16x32_bf16 v[94:97], v[160:163], v[200:203], v[94:97]
	v_mfma_f32_16x16x32_bf16 v[86:89], v[146:149], v[208:211], v[86:89]
	v_mfma_f32_16x16x32_bf16 v[78:81], v[160:163], v[208:211], v[78:81]
	v_mfma_f32_16x16x32_bf16 v[126:129], v[156:159], v[188:191], v[126:129]
	v_mfma_f32_16x16x32_bf16 v[122:125], v[164:167], v[188:191], v[122:125]
	v_mfma_f32_16x16x32_bf16 v[118:121], v[156:159], v[196:199], v[118:121]
	v_mfma_f32_16x16x32_bf16 v[110:113], v[164:167], v[196:199], v[110:113]
	v_mfma_f32_16x16x32_bf16 v[102:105], v[156:159], v[204:207], v[102:105]
	v_mfma_f32_16x16x32_bf16 v[94:97], v[164:167], v[204:207], v[94:97]
	v_mfma_f32_16x16x32_bf16 v[86:89], v[156:159], v[212:215], v[86:89]
	v_mfma_f32_16x16x32_bf16 v[78:81], v[164:167], v[212:215], v[78:81]
	v_mfma_f32_16x16x32_bf16 v[114:117], v[168:171], v[184:187], v[114:117]
	v_mfma_f32_16x16x32_bf16 v[106:109], v[176:179], v[184:187], v[106:109]
	v_mfma_f32_16x16x32_bf16 v[98:101], v[168:171], v[192:195], v[98:101]
	v_mfma_f32_16x16x32_bf16 v[90:93], v[176:179], v[192:195], v[90:93]
	v_mfma_f32_16x16x32_bf16 v[82:85], v[168:171], v[200:203], v[82:85]
	v_mfma_f32_16x16x32_bf16 v[74:77], v[176:179], v[200:203], v[74:77]
	v_mfma_f32_16x16x32_bf16 v[70:73], v[168:171], v[208:211], v[70:73]
	v_mfma_f32_16x16x32_bf16 v[66:69], v[176:179], v[208:211], v[66:69]
	v_mfma_f32_16x16x32_bf16 v[114:117], v[172:175], v[188:191], v[114:117]
	v_mfma_f32_16x16x32_bf16 v[106:109], v[180:183], v[188:191], v[106:109]
	v_mfma_f32_16x16x32_bf16 v[98:101], v[172:175], v[196:199], v[98:101]
	v_mfma_f32_16x16x32_bf16 v[90:93], v[180:183], v[196:199], v[90:93]
	v_mfma_f32_16x16x32_bf16 v[82:85], v[172:175], v[204:207], v[82:85]
	v_mfma_f32_16x16x32_bf16 v[74:77], v[180:183], v[204:207], v[74:77]
	v_mfma_f32_16x16x32_bf16 v[70:73], v[172:175], v[212:215], v[70:73]
	v_mfma_f32_16x16x32_bf16 v[66:69], v[180:183], v[212:215], v[66:69]
	s_setprio 0
	s_barrier
	s_add_i32 s70, s61, s33
	v_lshl_add_u64 v[216:217], s[24:25], 0, v[134:135]
	s_mov_b32 m0, s70
	ds_read_b128 v[184:187], v154 offset:16384
	ds_read_b128 v[188:191], v154 offset:17408
	ds_read_b128 v[192:195], v154 offset:18432
	ds_read_b128 v[196:199], v154 offset:19456
	ds_read_b128 v[200:203], v154 offset:20480
	ds_read_b128 v[204:207], v154 offset:21504
	ds_read_b128 v[208:211], v154 offset:22528
	ds_read_b128 v[212:215], v154 offset:23552
	global_load_lds_dwordx4 v134, s[24:25]
	s_add_i32 m0, s70, 0x2000
	s_add_u32 s70, s24, 0x80000
	v_lshl_add_u64 v[218:219], s[24:25], 0, v[130:131]
	s_addc_u32 s71, s25, 0
	s_add_i32 s72, s62, s33
	global_load_lds_dwordx4 v130, s[24:25]
	s_mov_b32 m0, s72
	v_lshl_add_u64 v[222:223], s[26:27], 0, v[132:133]
	global_load_lds_dwordx4 v134, s[70:71]
	s_add_i32 m0, s72, 0x2000
	s_nop 0
	global_load_lds_dwordx4 v130, s[70:71]
	v_lshl_add_u64 v[220:221], s[26:27], 0, v[136:137]
	s_mov_b32 m0, s21
	s_nop 0
	global_load_lds_dwordx4 v136, s[26:27]
	s_mov_b32 m0, s36
	s_nop 0
	global_load_lds_dwordx4 v132, s[26:27]
	s_waitcnt vmcnt(8)
	s_waitcnt lgkmcnt(0)
	s_barrier
	s_setprio 1
	v_mfma_f32_16x16x32_bf16 v[62:65], v[146:149], v[184:187], v[62:65]
	v_mfma_f32_16x16x32_bf16 v[58:61], v[160:163], v[184:187], v[58:61]
	v_mfma_f32_16x16x32_bf16 v[54:57], v[146:149], v[192:195], v[54:57]
	v_mfma_f32_16x16x32_bf16 v[46:49], v[160:163], v[192:195], v[46:49]
	v_mfma_f32_16x16x32_bf16 v[38:41], v[146:149], v[200:203], v[38:41]
	v_mfma_f32_16x16x32_bf16 v[30:33], v[160:163], v[200:203], v[30:33]
	v_mfma_f32_16x16x32_bf16 v[22:25], v[146:149], v[208:211], v[22:25]
	v_mfma_f32_16x16x32_bf16 v[14:17], v[160:163], v[208:211], v[14:17]
	v_mfma_f32_16x16x32_bf16 v[62:65], v[156:159], v[188:191], v[62:65]
	v_mfma_f32_16x16x32_bf16 v[58:61], v[164:167], v[188:191], v[58:61]
	v_mfma_f32_16x16x32_bf16 v[54:57], v[156:159], v[196:199], v[54:57]
	v_mfma_f32_16x16x32_bf16 v[46:49], v[164:167], v[196:199], v[46:49]
	v_mfma_f32_16x16x32_bf16 v[38:41], v[156:159], v[204:207], v[38:41]
	v_mfma_f32_16x16x32_bf16 v[30:33], v[164:167], v[204:207], v[30:33]
	v_mfma_f32_16x16x32_bf16 v[22:25], v[156:159], v[212:215], v[22:25]
	v_mfma_f32_16x16x32_bf16 v[14:17], v[164:167], v[212:215], v[14:17]
	v_mfma_f32_16x16x32_bf16 v[50:53], v[168:171], v[184:187], v[50:53]
	v_mfma_f32_16x16x32_bf16 v[42:45], v[176:179], v[184:187], v[42:45]
	v_mfma_f32_16x16x32_bf16 v[34:37], v[168:171], v[192:195], v[34:37]
	v_mfma_f32_16x16x32_bf16 v[26:29], v[176:179], v[192:195], v[26:29]
	v_mfma_f32_16x16x32_bf16 v[18:21], v[168:171], v[200:203], v[18:21]
	v_mfma_f32_16x16x32_bf16 v[10:13], v[176:179], v[200:203], v[10:13]
	v_mfma_f32_16x16x32_bf16 v[6:9], v[168:171], v[208:211], v[6:9]
	v_mfma_f32_16x16x32_bf16 v[2:5], v[176:179], v[208:211], v[2:5]
	v_mfma_f32_16x16x32_bf16 v[50:53], v[172:175], v[188:191], v[50:53]
	v_mfma_f32_16x16x32_bf16 v[42:45], v[180:183], v[188:191], v[42:45]
	v_mfma_f32_16x16x32_bf16 v[34:37], v[172:175], v[196:199], v[34:37]
	v_mfma_f32_16x16x32_bf16 v[26:29], v[180:183], v[196:199], v[26:29]
	v_mfma_f32_16x16x32_bf16 v[18:21], v[172:175], v[204:207], v[18:21]
	v_mfma_f32_16x16x32_bf16 v[10:13], v[180:183], v[204:207], v[10:13]
	v_mfma_f32_16x16x32_bf16 v[6:9], v[172:175], v[212:215], v[6:9]
	v_mfma_f32_16x16x32_bf16 v[2:5], v[180:183], v[212:215], v[2:5]
	s_setprio 0
	s_barrier
	s_add_i32 s70, 0, 0x18000
	v_add_u32_e32 v155, s70, v150
	s_add_i32 s71, 0, 0x1c000
	ds_read_b128 v[146:149], v155
	ds_read_b128 v[156:159], v155 offset:1024
	ds_read_b128 v[160:163], v155 offset:2048
	ds_read_b128 v[164:167], v155 offset:3072
	v_add_u32_e32 v155, s71, v150
	ds_read_b128 v[168:171], v155
	ds_read_b128 v[172:175], v155 offset:1024
	ds_read_b128 v[176:179], v155 offset:2048
	ds_read_b128 v[180:183], v155 offset:3072
	s_add_u32 s26, s26, 0x80000
	s_addc_u32 s27, s27, 0
	s_mov_b32 m0, s37
	ds_read_b128 v[184:187], v154 offset:32768
	ds_read_b128 v[188:191], v154 offset:33792
	ds_read_b128 v[192:195], v154 offset:34816
	ds_read_b128 v[196:199], v154 offset:35840
	ds_read_b128 v[200:203], v154 offset:36864
	ds_read_b128 v[204:207], v154 offset:37888
	ds_read_b128 v[208:211], v154 offset:38912
	ds_read_b128 v[212:215], v154 offset:39936
	global_load_lds_dwordx4 v136, s[26:27]
	s_mov_b32 m0, s42
	s_nop 0
	global_load_lds_dwordx4 v132, s[26:27]
	s_waitcnt vmcnt(8)
	s_waitcnt lgkmcnt(0)
	s_barrier
	s_setprio 1
	v_mfma_f32_16x16x32_bf16 v[126:129], v[146:149], v[184:187], v[126:129]
	v_mfma_f32_16x16x32_bf16 v[122:125], v[160:163], v[184:187], v[122:125]
	v_mfma_f32_16x16x32_bf16 v[118:121], v[146:149], v[192:195], v[118:121]
	v_mfma_f32_16x16x32_bf16 v[110:113], v[160:163], v[192:195], v[110:113]
	v_mfma_f32_16x16x32_bf16 v[102:105], v[146:149], v[200:203], v[102:105]
	v_mfma_f32_16x16x32_bf16 v[94:97], v[160:163], v[200:203], v[94:97]
	v_mfma_f32_16x16x32_bf16 v[86:89], v[146:149], v[208:211], v[86:89]
	v_mfma_f32_16x16x32_bf16 v[78:81], v[160:163], v[208:211], v[78:81]
	v_mfma_f32_16x16x32_bf16 v[126:129], v[156:159], v[188:191], v[126:129]
	v_mfma_f32_16x16x32_bf16 v[122:125], v[164:167], v[188:191], v[122:125]
	v_mfma_f32_16x16x32_bf16 v[118:121], v[156:159], v[196:199], v[118:121]
	v_mfma_f32_16x16x32_bf16 v[110:113], v[164:167], v[196:199], v[110:113]
	v_mfma_f32_16x16x32_bf16 v[102:105], v[156:159], v[204:207], v[102:105]
	v_mfma_f32_16x16x32_bf16 v[94:97], v[164:167], v[204:207], v[94:97]
	v_mfma_f32_16x16x32_bf16 v[86:89], v[156:159], v[212:215], v[86:89]
	v_mfma_f32_16x16x32_bf16 v[78:81], v[164:167], v[212:215], v[78:81]
	v_mfma_f32_16x16x32_bf16 v[114:117], v[168:171], v[184:187], v[114:117]
	v_mfma_f32_16x16x32_bf16 v[106:109], v[176:179], v[184:187], v[106:109]
	v_mfma_f32_16x16x32_bf16 v[98:101], v[168:171], v[192:195], v[98:101]
	v_mfma_f32_16x16x32_bf16 v[90:93], v[176:179], v[192:195], v[90:93]
	v_mfma_f32_16x16x32_bf16 v[82:85], v[168:171], v[200:203], v[82:85]
	v_mfma_f32_16x16x32_bf16 v[74:77], v[176:179], v[200:203], v[74:77]
	v_mfma_f32_16x16x32_bf16 v[70:73], v[168:171], v[208:211], v[70:73]
	v_mfma_f32_16x16x32_bf16 v[66:69], v[176:179], v[208:211], v[66:69]
	v_mfma_f32_16x16x32_bf16 v[114:117], v[172:175], v[188:191], v[114:117]
	v_mfma_f32_16x16x32_bf16 v[106:109], v[180:183], v[188:191], v[106:109]
	v_mfma_f32_16x16x32_bf16 v[98:101], v[172:175], v[196:199], v[98:101]
	v_mfma_f32_16x16x32_bf16 v[90:93], v[180:183], v[196:199], v[90:93]
	v_mfma_f32_16x16x32_bf16 v[82:85], v[172:175], v[204:207], v[82:85]
	v_mfma_f32_16x16x32_bf16 v[74:77], v[180:183], v[204:207], v[74:77]
	v_mfma_f32_16x16x32_bf16 v[70:73], v[172:175], v[212:215], v[70:73]
	v_mfma_f32_16x16x32_bf16 v[66:69], v[180:183], v[212:215], v[66:69]
	s_setprio 0
	s_barrier
	s_add_i32 s26, s70, s33
	v_lshl_add_u64 v[216:217], v[216:217], 0, s[8:9]
	s_mov_b32 m0, s26
	ds_read_b128 v[184:187], v154 offset:49152
	ds_read_b128 v[188:191], v154 offset:50176
	ds_read_b128 v[192:195], v154 offset:51200
	ds_read_b128 v[196:199], v154 offset:52224
	ds_read_b128 v[200:203], v154 offset:53248
	ds_read_b128 v[204:207], v154 offset:54272
	ds_read_b128 v[208:211], v154 offset:55296
	ds_read_b128 v[212:215], v154 offset:56320
	global_load_lds_dwordx4 v[216:217], off
	s_add_i32 m0, s26, 0x2000
	s_add_u32 s24, s24, 0x80080
	v_lshl_add_u64 v[216:217], v[218:219], 0, s[8:9]
	s_addc_u32 s25, s25, 0
	s_add_i32 s26, s71, s33
	global_load_lds_dwordx4 v[216:217], off
	s_mov_b32 m0, s26
	s_nop 0
	global_load_lds_dwordx4 v134, s[24:25]
	s_add_i32 m0, s26, 0x2000
	s_nop 0
	global_load_lds_dwordx4 v130, s[24:25]
	v_lshl_add_u64 v[216:217], v[220:221], 0, s[8:9]
	s_mov_b32 m0, s44
	s_nop 0
	global_load_lds_dwordx4 v[216:217], off
	v_lshl_add_u64 v[216:217], v[222:223], 0, s[8:9]
	s_mov_b32 m0, s45
	s_nop 0
	global_load_lds_dwordx4 v[216:217], off
	s_waitcnt vmcnt(8)
	s_waitcnt lgkmcnt(0)
	s_barrier
	s_setprio 1
	v_mfma_f32_16x16x32_bf16 v[62:65], v[146:149], v[184:187], v[62:65]
	v_mfma_f32_16x16x32_bf16 v[58:61], v[160:163], v[184:187], v[58:61]
	v_mfma_f32_16x16x32_bf16 v[54:57], v[146:149], v[192:195], v[54:57]
	v_mfma_f32_16x16x32_bf16 v[46:49], v[160:163], v[192:195], v[46:49]
	v_mfma_f32_16x16x32_bf16 v[38:41], v[146:149], v[200:203], v[38:41]
	v_mfma_f32_16x16x32_bf16 v[30:33], v[160:163], v[200:203], v[30:33]
	v_mfma_f32_16x16x32_bf16 v[22:25], v[146:149], v[208:211], v[22:25]
	v_mfma_f32_16x16x32_bf16 v[14:17], v[160:163], v[208:211], v[14:17]
	v_mfma_f32_16x16x32_bf16 v[62:65], v[156:159], v[188:191], v[62:65]
	v_mfma_f32_16x16x32_bf16 v[58:61], v[164:167], v[188:191], v[58:61]
	v_mfma_f32_16x16x32_bf16 v[54:57], v[156:159], v[196:199], v[54:57]
	v_mfma_f32_16x16x32_bf16 v[46:49], v[164:167], v[196:199], v[46:49]
	v_mfma_f32_16x16x32_bf16 v[38:41], v[156:159], v[204:207], v[38:41]
	v_mfma_f32_16x16x32_bf16 v[30:33], v[164:167], v[204:207], v[30:33]
	v_mfma_f32_16x16x32_bf16 v[22:25], v[156:159], v[212:215], v[22:25]
	v_mfma_f32_16x16x32_bf16 v[14:17], v[164:167], v[212:215], v[14:17]
	v_mfma_f32_16x16x32_bf16 v[50:53], v[168:171], v[184:187], v[50:53]
	v_mfma_f32_16x16x32_bf16 v[42:45], v[176:179], v[184:187], v[42:45]
	v_mfma_f32_16x16x32_bf16 v[34:37], v[168:171], v[192:195], v[34:37]
	v_mfma_f32_16x16x32_bf16 v[26:29], v[176:179], v[192:195], v[26:29]
	v_mfma_f32_16x16x32_bf16 v[18:21], v[168:171], v[200:203], v[18:21]
	v_mfma_f32_16x16x32_bf16 v[10:13], v[176:179], v[200:203], v[10:13]
	v_mfma_f32_16x16x32_bf16 v[6:9], v[168:171], v[208:211], v[6:9]
	v_mfma_f32_16x16x32_bf16 v[2:5], v[176:179], v[208:211], v[2:5]
	v_mfma_f32_16x16x32_bf16 v[50:53], v[172:175], v[188:191], v[50:53]
	v_mfma_f32_16x16x32_bf16 v[42:45], v[180:183], v[188:191], v[42:45]
	v_mfma_f32_16x16x32_bf16 v[34:37], v[172:175], v[196:199], v[34:37]
	v_mfma_f32_16x16x32_bf16 v[26:29], v[180:183], v[196:199], v[26:29]
	v_mfma_f32_16x16x32_bf16 v[18:21], v[172:175], v[204:207], v[18:21]
	v_mfma_f32_16x16x32_bf16 v[10:13], v[180:183], v[204:207], v[10:13]
	v_mfma_f32_16x16x32_bf16 v[6:9], v[172:175], v[212:215], v[6:9]
	v_mfma_f32_16x16x32_bf16 v[2:5], v[180:183], v[212:215], v[2:5]
	s_setprio 0
	s_barrier
	s_add_i32 s69, s69, 2
	s_add_u32 s22, s22, 0x100
	s_addc_u32 s23, s23, 0
	s_add_u32 s67, s67, 0x100
	s_addc_u32 s68, s68, 0
	s_cmp_gt_u32 s69, 29
	s_cbranch_scc0 .LBB0_767
	s_nop 0
	s_nop 0
	s_nop 0
	s_nop 0
	s_nop 0
	s_nop 0
	s_nop 0
	s_nop 0
	s_nop 0
	s_nop 0
	s_nop 0
	s_nop 0
	s_and_b64 vcc, exec, s[10:11]
	s_cbranch_vccz .LBB0_770
	s_barrier

.LBB0_1043:
	ds_read_b128 v[26:29], v209
	ds_read_b128 v[30:33], v209 offset:1024
	ds_read_b128 v[18:21], v209 offset:2048
	ds_read_b128 v[22:25], v209 offset:3072
	ds_read_b128 v[10:13], v210
	ds_read_b128 v[14:17], v210 offset:1024
	ds_read_b128 v[2:5], v210 offset:2048
	ds_read_b128 v[6:9], v210 offset:3072
	s_add_u32 s44, s40, 0xfffc0080
	s_addc_u32 s45, s41, -1
	s_cmp_eq_u32 s81, 12
	s_cselect_b32 s49, s1, s45
	s_cselect_b32 s48, s35, s44
	s_cselect_b32 s45, s31, s61
	s_cselect_b32 s44, s43, s60
	s_add_i32 m0, s65, 0xc000
	ds_read_b128 v[182:185], v211
	ds_read_b128 v[186:189], v211 offset:1024
	ds_read_b128 v[190:193], v211 offset:2048
	ds_read_b128 v[194:197], v211 offset:3072
	ds_read_b128 v[218:221], v211 offset:4096
	ds_read_b128 v[222:225], v211 offset:5120
	ds_read_b128 v[226:229], v211 offset:6144
	ds_read_b128 v[230:233], v211 offset:7168
	global_load_lds_dwordx4 v174, s[40:41]
	s_add_i32 m0, s65, 0xe000
	s_nop 0
	global_load_lds_dwordx4 v176, s[40:41]
	s_waitcnt vmcnt(8)
	s_waitcnt lgkmcnt(0)
	s_barrier
	s_setprio 1
	v_mfma_scale_f32_16x16x128_f8f6f4 v[158:161], v[26:33], v[182:189], v[158:161], v212, v213 op_sel_hi:[0,0,0]
	v_mfma_scale_f32_16x16x128_f8f6f4 v[154:157], v[18:25], v[182:189], v[154:157], v212, v213 op_sel_hi:[0,0,0]
	v_mfma_scale_f32_16x16x128_f8f6f4 v[142:145], v[26:33], v[190:197], v[142:145], v212, v213 op_sel_hi:[0,0,0]
	v_mfma_scale_f32_16x16x128_f8f6f4 v[138:141], v[18:25], v[190:197], v[138:141], v212, v213 op_sel_hi:[0,0,0]
	v_mfma_scale_f32_16x16x128_f8f6f4 v[126:129], v[26:33], v[218:225], v[126:129], v212, v213 op_sel_hi:[0,0,0]
	v_mfma_scale_f32_16x16x128_f8f6f4 v[122:125], v[18:25], v[218:225], v[122:125], v212, v213 op_sel_hi:[0,0,0]
	v_mfma_scale_f32_16x16x128_f8f6f4 v[110:113], v[26:33], v[226:233], v[110:113], v212, v213 op_sel_hi:[0,0,0]
	v_mfma_scale_f32_16x16x128_f8f6f4 v[106:109], v[18:25], v[226:233], v[106:109], v212, v213 op_sel_hi:[0,0,0]
	v_mfma_scale_f32_16x16x128_f8f6f4 v[150:153], v[10:17], v[182:189], v[150:153], v212, v213 op_sel_hi:[0,0,0]
	v_mfma_scale_f32_16x16x128_f8f6f4 v[146:149], v[2:9], v[182:189], v[146:149], v212, v213 op_sel_hi:[0,0,0]
	v_mfma_scale_f32_16x16x128_f8f6f4 v[134:137], v[10:17], v[190:197], v[134:137], v212, v213 op_sel_hi:[0,0,0]
	v_mfma_scale_f32_16x16x128_f8f6f4 v[130:133], v[2:9], v[190:197], v[130:133], v212, v213 op_sel_hi:[0,0,0]
	v_mfma_scale_f32_16x16x128_f8f6f4 v[118:121], v[10:17], v[218:225], v[118:121], v212, v213 op_sel_hi:[0,0,0]
	v_mfma_scale_f32_16x16x128_f8f6f4 v[114:117], v[2:9], v[218:225], v[114:117], v212, v213 op_sel_hi:[0,0,0]
	v_mfma_scale_f32_16x16x128_f8f6f4 v[102:105], v[10:17], v[226:233], v[102:105], v212, v213 op_sel_hi:[0,0,0]
	v_mfma_scale_f32_16x16x128_f8f6f4 v[98:101], v[2:9], v[226:233], v[98:101], v212, v213 op_sel_hi:[0,0,0]
	s_setprio 0
	s_barrier
	s_add_i32 s82, s77, s64
	v_lshl_add_u64 v[182:183], s[44:45], 0, v[164:165]
	s_mov_b32 m0, s82
	ds_read_b128 v[190:193], v211 offset:16384
	ds_read_b128 v[194:197], v211 offset:17408
	ds_read_b128 v[218:221], v211 offset:18432
	ds_read_b128 v[222:225], v211 offset:19456
	ds_read_b128 v[226:229], v211 offset:20480
	ds_read_b128 v[230:233], v211 offset:21504
	ds_read_b128 v[234:237], v211 offset:22528
	ds_read_b128 v[238:241], v211 offset:23552
	global_load_lds_dwordx4 v164, s[44:45]
	s_add_i32 m0, s82, 0x2000
	s_add_u32 s82, s44, 0x40000
	v_lshl_add_u64 v[184:185], s[44:45], 0, v[168:169]
	s_addc_u32 s83, s45, 0
	s_add_i32 s84, s78, s64
	global_load_lds_dwordx4 v168, s[44:45]
	s_mov_b32 m0, s84
	v_lshl_add_u64 v[188:189], s[48:49], 0, v[166:167]
	global_load_lds_dwordx4 v164, s[82:83]
	s_add_i32 m0, s84, 0x2000
	s_nop 0
	global_load_lds_dwordx4 v168, s[82:83]
	v_lshl_add_u64 v[186:187], s[48:49], 0, v[162:163]
	s_mov_b32 m0, s65
	s_nop 0
	global_load_lds_dwordx4 v162, s[48:49]
	s_mov_b32 m0, s66
	s_nop 0
	global_load_lds_dwordx4 v166, s[48:49]
	s_waitcnt vmcnt(8)
	s_waitcnt lgkmcnt(0)
	s_barrier
	s_setprio 1
	v_mfma_scale_f32_16x16x128_f8f6f4 v[94:97], v[26:33], v[190:197], v[94:97], v212, v213 op_sel_hi:[0,0,0]
	v_mfma_scale_f32_16x16x128_f8f6f4 v[90:93], v[18:25], v[190:197], v[90:93], v212, v213 op_sel_hi:[0,0,0]
	v_mfma_scale_f32_16x16x128_f8f6f4 v[78:81], v[26:33], v[218:225], v[78:81], v212, v213 op_sel_hi:[0,0,0]
	v_mfma_scale_f32_16x16x128_f8f6f4 v[74:77], v[18:25], v[218:225], v[74:77], v212, v213 op_sel_hi:[0,0,0]
	v_mfma_scale_f32_16x16x128_f8f6f4 v[62:65], v[26:33], v[226:233], v[62:65], v212, v213 op_sel_hi:[0,0,0]
	v_mfma_scale_f32_16x16x128_f8f6f4 v[58:61], v[18:25], v[226:233], v[58:61], v212, v213 op_sel_hi:[0,0,0]
	v_mfma_scale_f32_16x16x128_f8f6f4 v[46:49], v[26:33], v[234:241], v[46:49], v212, v213 op_sel_hi:[0,0,0]
	v_mfma_scale_f32_16x16x128_f8f6f4 v[42:45], v[18:25], v[234:241], v[42:45], v212, v213 op_sel_hi:[0,0,0]
	v_mfma_scale_f32_16x16x128_f8f6f4 v[86:89], v[10:17], v[190:197], v[86:89], v212, v213 op_sel_hi:[0,0,0]
	v_mfma_scale_f32_16x16x128_f8f6f4 v[82:85], v[2:9], v[190:197], v[82:85], v212, v213 op_sel_hi:[0,0,0]
	v_mfma_scale_f32_16x16x128_f8f6f4 v[70:73], v[10:17], v[218:225], v[70:73], v212, v213 op_sel_hi:[0,0,0]
	v_mfma_scale_f32_16x16x128_f8f6f4 v[66:69], v[2:9], v[218:225], v[66:69], v212, v213 op_sel_hi:[0,0,0]
	v_mfma_scale_f32_16x16x128_f8f6f4 v[54:57], v[10:17], v[226:233], v[54:57], v212, v213 op_sel_hi:[0,0,0]
	v_mfma_scale_f32_16x16x128_f8f6f4 v[50:53], v[2:9], v[226:233], v[50:53], v212, v213 op_sel_hi:[0,0,0]
	v_mfma_scale_f32_16x16x128_f8f6f4 v[38:41], v[10:17], v[234:241], v[38:41], v212, v213 op_sel_hi:[0,0,0]
	v_mfma_scale_f32_16x16x128_f8f6f4 v[34:37], v[2:9], v[234:241], v[34:37], v212, v213 op_sel_hi:[0,0,0]
	s_setprio 0
	s_barrier
	s_add_i32 s82, 0, 0x18000
	s_add_i32 s83, 0, 0x1c000
	v_add_u32_e32 v14, s82, v202
	v_add_u32_e32 v30, s83, v202
	ds_read_b128 v[2:5], v14
	ds_read_b128 v[6:9], v14 offset:1024
	ds_read_b128 v[10:13], v14 offset:2048
	ds_read_b128 v[14:17], v14 offset:3072
	ds_read_b128 v[18:21], v30
	ds_read_b128 v[22:25], v30 offset:1024
	ds_read_b128 v[26:29], v30 offset:2048
	ds_read_b128 v[30:33], v30 offset:3072
	s_add_u32 s48, s48, 0x40000
	s_addc_u32 s49, s49, 0
	s_mov_b32 m0, s67
	ds_read_b128 v[190:193], v211 offset:32768
	ds_read_b128 v[194:197], v211 offset:33792
	ds_read_b128 v[218:221], v211 offset:34816
	ds_read_b128 v[222:225], v211 offset:35840
	ds_read_b128 v[226:229], v211 offset:36864
	ds_read_b128 v[230:233], v211 offset:37888
	ds_read_b128 v[234:237], v211 offset:38912
	ds_read_b128 v[238:241], v211 offset:39936
	global_load_lds_dwordx4 v162, s[48:49]
	s_mov_b32 m0, s68
	s_nop 0
	global_load_lds_dwordx4 v166, s[48:49]
	s_waitcnt vmcnt(8)
	s_waitcnt lgkmcnt(0)
	s_barrier
	s_setprio 1
	v_mfma_scale_f32_16x16x128_f8f6f4 v[158:161], v[2:9], v[190:197], v[158:161], v212, v213 op_sel_hi:[0,0,0]
	v_mfma_scale_f32_16x16x128_f8f6f4 v[154:157], v[10:17], v[190:197], v[154:157], v212, v213 op_sel_hi:[0,0,0]
	v_mfma_scale_f32_16x16x128_f8f6f4 v[142:145], v[2:9], v[218:225], v[142:145], v212, v213 op_sel_hi:[0,0,0]
	v_mfma_scale_f32_16x16x128_f8f6f4 v[138:141], v[10:17], v[218:225], v[138:141], v212, v213 op_sel_hi:[0,0,0]
	v_mfma_scale_f32_16x16x128_f8f6f4 v[126:129], v[2:9], v[226:233], v[126:129], v212, v213 op_sel_hi:[0,0,0]
	v_mfma_scale_f32_16x16x128_f8f6f4 v[122:125], v[10:17], v[226:233], v[122:125], v212, v213 op_sel_hi:[0,0,0]
	v_mfma_scale_f32_16x16x128_f8f6f4 v[110:113], v[2:9], v[234:241], v[110:113], v212, v213 op_sel_hi:[0,0,0]
	v_mfma_scale_f32_16x16x128_f8f6f4 v[106:109], v[10:17], v[234:241], v[106:109], v212, v213 op_sel_hi:[0,0,0]
	v_mfma_scale_f32_16x16x128_f8f6f4 v[150:153], v[18:25], v[190:197], v[150:153], v212, v213 op_sel_hi:[0,0,0]
	v_mfma_scale_f32_16x16x128_f8f6f4 v[146:149], v[26:33], v[190:197], v[146:149], v212, v213 op_sel_hi:[0,0,0]
	v_mfma_scale_f32_16x16x128_f8f6f4 v[134:137], v[18:25], v[218:225], v[134:137], v212, v213 op_sel_hi:[0,0,0]
	v_mfma_scale_f32_16x16x128_f8f6f4 v[130:133], v[26:33], v[218:225], v[130:133], v212, v213 op_sel_hi:[0,0,0]
	v_mfma_scale_f32_16x16x128_f8f6f4 v[118:121], v[18:25], v[226:233], v[118:121], v212, v213 op_sel_hi:[0,0,0]
	v_mfma_scale_f32_16x16x128_f8f6f4 v[114:117], v[26:33], v[226:233], v[114:117], v212, v213 op_sel_hi:[0,0,0]
	v_mfma_scale_f32_16x16x128_f8f6f4 v[102:105], v[18:25], v[234:241], v[102:105], v212, v213 op_sel_hi:[0,0,0]
	v_mfma_scale_f32_16x16x128_f8f6f4 v[98:101], v[26:33], v[234:241], v[98:101], v212, v213 op_sel_hi:[0,0,0]
	s_setprio 0
	s_barrier
	s_add_i32 s48, s82, s64
	v_lshl_add_u64 v[182:183], v[182:183], 0, s[24:25]
	s_mov_b32 m0, s48
	ds_read_b128 v[190:193], v211 offset:49152
	ds_read_b128 v[194:197], v211 offset:50176
	ds_read_b128 v[218:221], v211 offset:51200
	ds_read_b128 v[222:225], v211 offset:52224
	ds_read_b128 v[226:229], v211 offset:53248
	ds_read_b128 v[230:233], v211 offset:54272
	ds_read_b128 v[234:237], v211 offset:55296
	ds_read_b128 v[238:241], v211 offset:56320
	global_load_lds_dwordx4 v[182:183], off
	s_add_i32 m0, s48, 0x2000
	s_add_u32 s44, s44, 0x40080
	v_lshl_add_u64 v[182:183], v[184:185], 0, s[24:25]
	s_addc_u32 s45, s45, 0
	s_add_i32 s48, s83, s64
	global_load_lds_dwordx4 v[182:183], off
	s_mov_b32 m0, s48
	s_nop 0
	global_load_lds_dwordx4 v164, s[44:45]
	s_add_i32 m0, s48, 0x2000
	s_nop 0
	global_load_lds_dwordx4 v168, s[44:45]
	v_lshl_add_u64 v[182:183], v[186:187], 0, s[24:25]
	s_mov_b32 m0, s72
	s_nop 0
	global_load_lds_dwordx4 v[182:183], off
	v_lshl_add_u64 v[182:183], v[188:189], 0, s[24:25]
	s_mov_b32 m0, s73
	s_nop 0
	global_load_lds_dwordx4 v[182:183], off
	s_waitcnt vmcnt(8)
	s_waitcnt lgkmcnt(0)
	s_barrier
	s_setprio 1
	v_mfma_scale_f32_16x16x128_f8f6f4 v[94:97], v[2:9], v[190:197], v[94:97], v212, v213 op_sel_hi:[0,0,0]
	v_mfma_scale_f32_16x16x128_f8f6f4 v[90:93], v[10:17], v[190:197], v[90:93], v212, v213 op_sel_hi:[0,0,0]
	v_mfma_scale_f32_16x16x128_f8f6f4 v[78:81], v[2:9], v[218:225], v[78:81], v212, v213 op_sel_hi:[0,0,0]
	v_mfma_scale_f32_16x16x128_f8f6f4 v[74:77], v[10:17], v[218:225], v[74:77], v212, v213 op_sel_hi:[0,0,0]
	v_mfma_scale_f32_16x16x128_f8f6f4 v[62:65], v[2:9], v[226:233], v[62:65], v212, v213 op_sel_hi:[0,0,0]
	v_mfma_scale_f32_16x16x128_f8f6f4 v[58:61], v[10:17], v[226:233], v[58:61], v212, v213 op_sel_hi:[0,0,0]
	v_mfma_scale_f32_16x16x128_f8f6f4 v[46:49], v[2:9], v[234:241], v[46:49], v212, v213 op_sel_hi:[0,0,0]
	v_mfma_scale_f32_16x16x128_f8f6f4 v[42:45], v[10:17], v[234:241], v[42:45], v212, v213 op_sel_hi:[0,0,0]
	v_mfma_scale_f32_16x16x128_f8f6f4 v[86:89], v[18:25], v[190:197], v[86:89], v212, v213 op_sel_hi:[0,0,0]
	v_mfma_scale_f32_16x16x128_f8f6f4 v[82:85], v[26:33], v[190:197], v[82:85], v212, v213 op_sel_hi:[0,0,0]
	v_mfma_scale_f32_16x16x128_f8f6f4 v[70:73], v[18:25], v[218:225], v[70:73], v212, v213 op_sel_hi:[0,0,0]
	v_mfma_scale_f32_16x16x128_f8f6f4 v[66:69], v[26:33], v[218:225], v[66:69], v212, v213 op_sel_hi:[0,0,0]
	v_mfma_scale_f32_16x16x128_f8f6f4 v[54:57], v[18:25], v[226:233], v[54:57], v212, v213 op_sel_hi:[0,0,0]
	v_mfma_scale_f32_16x16x128_f8f6f4 v[50:53], v[26:33], v[226:233], v[50:53], v212, v213 op_sel_hi:[0,0,0]
	v_mfma_scale_f32_16x16x128_f8f6f4 v[38:41], v[18:25], v[234:241], v[38:41], v212, v213 op_sel_hi:[0,0,0]
	v_mfma_scale_f32_16x16x128_f8f6f4 v[34:37], v[26:33], v[234:241], v[34:37], v212, v213 op_sel_hi:[0,0,0]
	s_setprio 0
	s_barrier
	s_add_i32 s81, s81, 2
	s_add_u32 s40, s40, 0x100
	s_addc_u32 s41, s41, 0
	s_add_u32 s60, s60, 0x100
	s_addc_u32 s61, s61, 0
	s_cmp_gt_u32 s81, 13
	s_cbranch_scc0 .LBB0_1043
	s_nop 0
	s_nop 0
	s_nop 0
	s_nop 0
	s_nop 0
	s_nop 0
	s_nop 0
	s_nop 0
	s_nop 0
	s_nop 0
	s_nop 0
	s_nop 0
	s_and_b64 vcc, exec, s[26:27]
	s_cbranch_vccz .LBB0_1046
	s_barrier

.LBB0_1257:
	ds_read_b128 v[20:23], v202
	ds_read_b128 v[166:169], v202 offset:1024
	ds_read_b128 v[14:17], v202 offset:2048
	ds_read_b128 v[162:165], v202 offset:3072
	ds_read_b128 v[8:11], v203
	ds_read_b128 v[158:161], v203 offset:1024
	ds_read_b128 v[2:5], v203 offset:2048
	ds_read_b128 v[154:157], v203 offset:3072
	s_add_u32 s22, s20, 0xfffc0080
	s_addc_u32 s23, s21, -1
	s_cmp_eq_u32 s63, 12
	s_cselect_b32 s25, s11, s23
	s_cselect_b32 s24, s49, s22
	s_cselect_b32 s23, s13, s62
	s_cselect_b32 s22, s60, s61
	s_add_i32 m0, s35, 0xc000
	ds_read_b128 v[184:187], v204
	ds_read_b128 v[188:191], v204 offset:1024
	ds_read_b128 v[206:209], v204 offset:2048
	ds_read_b128 v[222:225], v204 offset:3072
	ds_read_b128 v[212:215], v204 offset:4096
	ds_read_b128 v[226:229], v204 offset:5120
	ds_read_b128 v[218:221], v204 offset:6144
	ds_read_b128 v[230:233], v204 offset:7168
	global_load_lds_dwordx4 v180, s[20:21]
	s_add_i32 m0, s35, 0xe000
	s_nop 0
	global_load_lds_dwordx4 v182, s[20:21]
	s_waitcnt vmcnt(8)
	s_waitcnt lgkmcnt(0)
	s_barrier
	s_setprio 1
	v_mov_b32_e32 v24, v166
	v_mov_b32_e32 v25, v167
	s_nop 1
	v_mfma_scale_f32_16x16x128_f8f6f4 v[150:153], v[20:25], v[184:189], v[150:153], v168, v190 op_sel_hi:[0,0,0] cbsz:2 blgp:2
	v_mov_b32_e32 v18, v162
	v_mov_b32_e32 v19, v163
	s_nop 1
	v_mfma_scale_f32_16x16x128_f8f6f4 v[138:141], v[14:19], v[184:189], v[138:141], v164, v190 op_sel_hi:[0,0,0] cbsz:2 blgp:2
	v_mov_b32_e32 v210, v222
	v_mov_b32_e32 v211, v223
	s_nop 1
	v_mfma_scale_f32_16x16x128_f8f6f4 v[134:137], v[20:25], v[206:211], v[134:137], v168, v224 op_sel_hi:[0,0,0] cbsz:2 blgp:2
	v_mfma_scale_f32_16x16x128_f8f6f4 v[122:125], v[14:19], v[206:211], v[122:125], v164, v224 op_sel_hi:[0,0,0] cbsz:2 blgp:2
	v_mov_b32_e32 v216, v226
	v_mov_b32_e32 v217, v227
	s_nop 1
	v_mfma_scale_f32_16x16x128_f8f6f4 v[118:121], v[20:25], v[212:217], v[118:121], v168, v228 op_sel_hi:[0,0,0] cbsz:2 blgp:2
	v_mfma_scale_f32_16x16x128_f8f6f4 v[106:109], v[14:19], v[212:217], v[106:109], v164, v228 op_sel_hi:[0,0,0] cbsz:2 blgp:2
	v_mov_b32_e32 v222, v230
	v_mov_b32_e32 v223, v231
	s_nop 1
	v_mfma_scale_f32_16x16x128_f8f6f4 v[102:105], v[20:25], v[218:223], v[102:105], v168, v232 op_sel_hi:[0,0,0] cbsz:2 blgp:2
	v_mfma_scale_f32_16x16x128_f8f6f4 v[90:93], v[14:19], v[218:223], v[90:93], v164, v232 op_sel_hi:[0,0,0] cbsz:2 blgp:2
	v_mov_b32_e32 v12, v158
	v_mov_b32_e32 v13, v159
	s_nop 1
	v_mfma_scale_f32_16x16x128_f8f6f4 v[146:149], v[8:13], v[184:189], v[146:149], v160, v190 op_sel_hi:[0,0,0] cbsz:2 blgp:2
	v_mov_b32_e32 v6, v154
	v_mov_b32_e32 v7, v155
	s_nop 1
	v_mfma_scale_f32_16x16x128_f8f6f4 v[142:145], v[2:7], v[184:189], v[142:145], v156, v190 op_sel_hi:[0,0,0] cbsz:2 blgp:2
	v_mfma_scale_f32_16x16x128_f8f6f4 v[130:133], v[8:13], v[206:211], v[130:133], v160, v224 op_sel_hi:[0,0,0] cbsz:2 blgp:2
	v_mfma_scale_f32_16x16x128_f8f6f4 v[126:129], v[2:7], v[206:211], v[126:129], v156, v224 op_sel_hi:[0,0,0] cbsz:2 blgp:2
	v_mfma_scale_f32_16x16x128_f8f6f4 v[114:117], v[8:13], v[212:217], v[114:117], v160, v228 op_sel_hi:[0,0,0] cbsz:2 blgp:2
	v_mfma_scale_f32_16x16x128_f8f6f4 v[110:113], v[2:7], v[212:217], v[110:113], v156, v228 op_sel_hi:[0,0,0] cbsz:2 blgp:2
	v_mfma_scale_f32_16x16x128_f8f6f4 v[98:101], v[8:13], v[218:223], v[98:101], v160, v232 op_sel_hi:[0,0,0] cbsz:2 blgp:2
	v_mfma_scale_f32_16x16x128_f8f6f4 v[94:97], v[2:7], v[218:223], v[94:97], v156, v232 op_sel_hi:[0,0,0] cbsz:2 blgp:2
	s_setprio 0
	s_barrier
	s_add_i32 s64, s42, s27
	v_lshl_add_u64 v[184:185], s[22:23], 0, v[172:173]
	s_mov_b32 m0, s64
	ds_read_b128 v[206:209], v204 offset:16384
	ds_read_b128 v[228:231], v204 offset:17408
	ds_read_b128 v[212:215], v204 offset:18432
	ds_read_b128 v[232:235], v204 offset:19456
	ds_read_b128 v[218:221], v204 offset:20480
	ds_read_b128 v[236:239], v204 offset:21504
	ds_read_b128 v[224:227], v204 offset:22528
	ds_read_b128 v[240:243], v204 offset:23552
	global_load_lds_dwordx4 v172, s[22:23]
	s_add_i32 m0, s64, 0x2000
	s_add_u32 s64, s22, 0x40000
	v_lshl_add_u64 v[186:187], s[22:23], 0, v[174:175]
	s_addc_u32 s65, s23, 0
	s_add_i32 s66, s43, s27
	global_load_lds_dwordx4 v174, s[22:23]
	s_mov_b32 m0, s66
	v_lshl_add_u64 v[188:189], s[24:25], 0, v[178:179]
	global_load_lds_dwordx4 v172, s[64:65]
	s_add_i32 m0, s66, 0x2000
	v_lshl_add_u64 v[190:191], s[24:25], 0, v[176:177]
	global_load_lds_dwordx4 v174, s[64:65]
	s_mov_b32 m0, s35
	s_nop 0
	global_load_lds_dwordx4 v178, s[24:25]
	s_mov_b32 m0, s36
	s_nop 0
	global_load_lds_dwordx4 v176, s[24:25]
	s_waitcnt vmcnt(8)
	s_waitcnt lgkmcnt(0)
	s_barrier
	s_setprio 1
	v_mov_b32_e32 v210, v228
	v_mov_b32_e32 v211, v229
	s_nop 1
	v_mfma_scale_f32_16x16x128_f8f6f4 v[86:89], v[20:25], v[206:211], v[86:89], v168, v230 op_sel_hi:[0,0,0] cbsz:2 blgp:2
	v_mfma_scale_f32_16x16x128_f8f6f4 v[74:77], v[14:19], v[206:211], v[74:77], v164, v230 op_sel_hi:[0,0,0] cbsz:2 blgp:2
	v_mov_b32_e32 v216, v232
	v_mov_b32_e32 v217, v233
	s_nop 1
	v_mfma_scale_f32_16x16x128_f8f6f4 v[70:73], v[20:25], v[212:217], v[70:73], v168, v234 op_sel_hi:[0,0,0] cbsz:2 blgp:2
	v_mfma_scale_f32_16x16x128_f8f6f4 v[58:61], v[14:19], v[212:217], v[58:61], v164, v234 op_sel_hi:[0,0,0] cbsz:2 blgp:2
	v_mov_b32_e32 v222, v236
	v_mov_b32_e32 v223, v237
	s_nop 1
	v_mfma_scale_f32_16x16x128_f8f6f4 v[54:57], v[20:25], v[218:223], v[54:57], v168, v238 op_sel_hi:[0,0,0] cbsz:2 blgp:2
	v_mfma_scale_f32_16x16x128_f8f6f4 v[42:45], v[14:19], v[218:223], v[42:45], v164, v238 op_sel_hi:[0,0,0] cbsz:2 blgp:2
	v_mov_b32_e32 v228, v240
	v_mov_b32_e32 v229, v241
	s_nop 1
	v_mfma_scale_f32_16x16x128_f8f6f4 v[38:41], v[20:25], v[224:229], v[38:41], v168, v242 op_sel_hi:[0,0,0] cbsz:2 blgp:2
	v_mfma_scale_f32_16x16x128_f8f6f4 v[26:29], v[14:19], v[224:229], v[26:29], v164, v242 op_sel_hi:[0,0,0] cbsz:2 blgp:2
	v_mfma_scale_f32_16x16x128_f8f6f4 v[82:85], v[8:13], v[206:211], v[82:85], v160, v230 op_sel_hi:[0,0,0] cbsz:2 blgp:2
	v_mfma_scale_f32_16x16x128_f8f6f4 v[78:81], v[2:7], v[206:211], v[78:81], v156, v230 op_sel_hi:[0,0,0] cbsz:2 blgp:2
	v_mfma_scale_f32_16x16x128_f8f6f4 v[66:69], v[8:13], v[212:217], v[66:69], v160, v234 op_sel_hi:[0,0,0] cbsz:2 blgp:2
	v_mfma_scale_f32_16x16x128_f8f6f4 v[62:65], v[2:7], v[212:217], v[62:65], v156, v234 op_sel_hi:[0,0,0] cbsz:2 blgp:2
	v_mfma_scale_f32_16x16x128_f8f6f4 v[50:53], v[8:13], v[218:223], v[50:53], v160, v238 op_sel_hi:[0,0,0] cbsz:2 blgp:2
	v_mfma_scale_f32_16x16x128_f8f6f4 v[46:49], v[2:7], v[218:223], v[46:49], v156, v238 op_sel_hi:[0,0,0] cbsz:2 blgp:2
	v_mfma_scale_f32_16x16x128_f8f6f4 v[34:37], v[8:13], v[224:229], v[34:37], v160, v242 op_sel_hi:[0,0,0] cbsz:2 blgp:2
	v_mfma_scale_f32_16x16x128_f8f6f4 v[30:33], v[2:7], v[224:229], v[30:33], v156, v242 op_sel_hi:[0,0,0] cbsz:2 blgp:2
	s_setprio 0
	s_barrier
	s_add_i32 s64, 0, 0x18000
	s_add_i32 s65, 0, 0x1c000
	v_add_u32_e32 v2, s64, v198
	v_add_u32_e32 v6, s65, v198
	ds_read_b128 v[20:23], v2
	ds_read_b128 v[166:169], v2 offset:1024
	ds_read_b128 v[14:17], v2 offset:2048
	ds_read_b128 v[162:165], v2 offset:3072
	ds_read_b128 v[8:11], v6
	ds_read_b128 v[154:157], v6 offset:1024
	ds_read_b128 v[2:5], v6 offset:2048
	ds_read_b128 v[158:161], v6 offset:3072
	s_add_u32 s24, s24, 0x40000
	s_addc_u32 s25, s25, 0
	s_mov_b32 m0, s37
	ds_read_b128 v[206:209], v204 offset:32768
	ds_read_b128 v[228:231], v204 offset:33792
	ds_read_b128 v[212:215], v204 offset:34816
	ds_read_b128 v[232:235], v204 offset:35840
	ds_read_b128 v[218:221], v204 offset:36864
	ds_read_b128 v[236:239], v204 offset:37888
	ds_read_b128 v[224:227], v204 offset:38912
	ds_read_b128 v[240:243], v204 offset:39936
	global_load_lds_dwordx4 v178, s[24:25]
	s_mov_b32 m0, s38
	s_nop 0
	global_load_lds_dwordx4 v176, s[24:25]
	s_waitcnt vmcnt(8)
	s_waitcnt lgkmcnt(0)
	s_barrier
	s_setprio 1
	v_mov_b32_e32 v24, v166
	v_mov_b32_e32 v25, v167
	v_mov_b32_e32 v210, v228
	v_mov_b32_e32 v211, v229
	s_nop 1
	v_mfma_scale_f32_16x16x128_f8f6f4 v[150:153], v[20:25], v[206:211], v[150:153], v168, v230 op_sel_hi:[0,0,0] cbsz:2 blgp:2
	v_mov_b32_e32 v18, v162
	v_mov_b32_e32 v19, v163
	s_nop 1
	v_mfma_scale_f32_16x16x128_f8f6f4 v[138:141], v[14:19], v[206:211], v[138:141], v164, v230 op_sel_hi:[0,0,0] cbsz:2 blgp:2
	v_mov_b32_e32 v216, v232
	v_mov_b32_e32 v217, v233
	s_nop 1
	v_mfma_scale_f32_16x16x128_f8f6f4 v[134:137], v[20:25], v[212:217], v[134:137], v168, v234 op_sel_hi:[0,0,0] cbsz:2 blgp:2
	v_mfma_scale_f32_16x16x128_f8f6f4 v[122:125], v[14:19], v[212:217], v[122:125], v164, v234 op_sel_hi:[0,0,0] cbsz:2 blgp:2
	v_mov_b32_e32 v222, v236
	v_mov_b32_e32 v223, v237
	s_nop 1
	v_mfma_scale_f32_16x16x128_f8f6f4 v[118:121], v[20:25], v[218:223], v[118:121], v168, v238 op_sel_hi:[0,0,0] cbsz:2 blgp:2
	v_mfma_scale_f32_16x16x128_f8f6f4 v[106:109], v[14:19], v[218:223], v[106:109], v164, v238 op_sel_hi:[0,0,0] cbsz:2 blgp:2
	v_mov_b32_e32 v228, v240
	v_mov_b32_e32 v229, v241
	s_nop 1
	v_mfma_scale_f32_16x16x128_f8f6f4 v[102:105], v[20:25], v[224:229], v[102:105], v168, v242 op_sel_hi:[0,0,0] cbsz:2 blgp:2
	v_mfma_scale_f32_16x16x128_f8f6f4 v[90:93], v[14:19], v[224:229], v[90:93], v164, v242 op_sel_hi:[0,0,0] cbsz:2 blgp:2
	v_mov_b32_e32 v12, v154
	v_mov_b32_e32 v13, v155
	s_nop 1
	v_mfma_scale_f32_16x16x128_f8f6f4 v[146:149], v[8:13], v[206:211], v[146:149], v156, v230 op_sel_hi:[0,0,0] cbsz:2 blgp:2
	v_mov_b32_e32 v6, v158
	v_mov_b32_e32 v7, v159
	s_nop 1
	v_mfma_scale_f32_16x16x128_f8f6f4 v[142:145], v[2:7], v[206:211], v[142:145], v160, v230 op_sel_hi:[0,0,0] cbsz:2 blgp:2
	v_mfma_scale_f32_16x16x128_f8f6f4 v[130:133], v[8:13], v[212:217], v[130:133], v156, v234 op_sel_hi:[0,0,0] cbsz:2 blgp:2
	v_mfma_scale_f32_16x16x128_f8f6f4 v[126:129], v[2:7], v[212:217], v[126:129], v160, v234 op_sel_hi:[0,0,0] cbsz:2 blgp:2
	v_mfma_scale_f32_16x16x128_f8f6f4 v[114:117], v[8:13], v[218:223], v[114:117], v156, v238 op_sel_hi:[0,0,0] cbsz:2 blgp:2
	v_mfma_scale_f32_16x16x128_f8f6f4 v[110:113], v[2:7], v[218:223], v[110:113], v160, v238 op_sel_hi:[0,0,0] cbsz:2 blgp:2
	v_mfma_scale_f32_16x16x128_f8f6f4 v[98:101], v[8:13], v[224:229], v[98:101], v156, v242 op_sel_hi:[0,0,0] cbsz:2 blgp:2
	v_mfma_scale_f32_16x16x128_f8f6f4 v[94:97], v[2:7], v[224:229], v[94:97], v160, v242 op_sel_hi:[0,0,0] cbsz:2 blgp:2
	s_setprio 0
	s_barrier
	s_add_i32 s24, s64, s27
	v_lshl_add_u64 v[154:155], v[184:185], 0, s[6:7]
	s_mov_b32 m0, s24
	ds_read_b128 v[206:209], v204 offset:49152
	ds_read_b128 v[228:231], v204 offset:50176
	ds_read_b128 v[212:215], v204 offset:51200
	ds_read_b128 v[232:235], v204 offset:52224
	ds_read_b128 v[218:221], v204 offset:53248
	ds_read_b128 v[236:239], v204 offset:54272
	ds_read_b128 v[224:227], v204 offset:55296
	ds_read_b128 v[240:243], v204 offset:56320
	global_load_lds_dwordx4 v[154:155], off
	s_add_i32 m0, s24, 0x2000
	s_add_u32 s22, s22, 0x40080
	v_lshl_add_u64 v[154:155], v[186:187], 0, s[6:7]
	s_addc_u32 s23, s23, 0
	s_add_i32 s24, s65, s27
	global_load_lds_dwordx4 v[154:155], off
	s_mov_b32 m0, s24
	s_nop 0
	global_load_lds_dwordx4 v172, s[22:23]
	s_add_i32 m0, s24, 0x2000
	s_nop 0
	global_load_lds_dwordx4 v174, s[22:23]
	v_lshl_add_u64 v[154:155], v[188:189], 0, s[6:7]
	s_mov_b32 m0, s39
	s_nop 0
	global_load_lds_dwordx4 v[154:155], off
	v_lshl_add_u64 v[154:155], v[190:191], 0, s[6:7]
	s_mov_b32 m0, s40
	s_nop 0
	global_load_lds_dwordx4 v[154:155], off
	s_waitcnt vmcnt(8)
	s_waitcnt lgkmcnt(0)
	s_barrier
	s_setprio 1
	v_mov_b32_e32 v210, v228
	v_mov_b32_e32 v211, v229
	s_nop 1
	v_mfma_scale_f32_16x16x128_f8f6f4 v[86:89], v[20:25], v[206:211], v[86:89], v168, v230 op_sel_hi:[0,0,0] cbsz:2 blgp:2
	v_mfma_scale_f32_16x16x128_f8f6f4 v[74:77], v[14:19], v[206:211], v[74:77], v164, v230 op_sel_hi:[0,0,0] cbsz:2 blgp:2
	v_mov_b32_e32 v216, v232
	v_mov_b32_e32 v217, v233
	s_nop 1
	v_mfma_scale_f32_16x16x128_f8f6f4 v[70:73], v[20:25], v[212:217], v[70:73], v168, v234 op_sel_hi:[0,0,0] cbsz:2 blgp:2
	v_mfma_scale_f32_16x16x128_f8f6f4 v[58:61], v[14:19], v[212:217], v[58:61], v164, v234 op_sel_hi:[0,0,0] cbsz:2 blgp:2
	v_mov_b32_e32 v222, v236
	v_mov_b32_e32 v223, v237
	s_nop 1
	v_mfma_scale_f32_16x16x128_f8f6f4 v[54:57], v[20:25], v[218:223], v[54:57], v168, v238 op_sel_hi:[0,0,0] cbsz:2 blgp:2
	v_mfma_scale_f32_16x16x128_f8f6f4 v[42:45], v[14:19], v[218:223], v[42:45], v164, v238 op_sel_hi:[0,0,0] cbsz:2 blgp:2
	v_mov_b32_e32 v228, v240
	v_mov_b32_e32 v229, v241
	s_nop 1
	v_mfma_scale_f32_16x16x128_f8f6f4 v[38:41], v[20:25], v[224:229], v[38:41], v168, v242 op_sel_hi:[0,0,0] cbsz:2 blgp:2
	v_mfma_scale_f32_16x16x128_f8f6f4 v[26:29], v[14:19], v[224:229], v[26:29], v164, v242 op_sel_hi:[0,0,0] cbsz:2 blgp:2
	v_mfma_scale_f32_16x16x128_f8f6f4 v[82:85], v[8:13], v[206:211], v[82:85], v156, v230 op_sel_hi:[0,0,0] cbsz:2 blgp:2
	v_mfma_scale_f32_16x16x128_f8f6f4 v[78:81], v[2:7], v[206:211], v[78:81], v160, v230 op_sel_hi:[0,0,0] cbsz:2 blgp:2
	v_mfma_scale_f32_16x16x128_f8f6f4 v[66:69], v[8:13], v[212:217], v[66:69], v156, v234 op_sel_hi:[0,0,0] cbsz:2 blgp:2
	v_mfma_scale_f32_16x16x128_f8f6f4 v[62:65], v[2:7], v[212:217], v[62:65], v160, v234 op_sel_hi:[0,0,0] cbsz:2 blgp:2
	v_mfma_scale_f32_16x16x128_f8f6f4 v[50:53], v[8:13], v[218:223], v[50:53], v156, v238 op_sel_hi:[0,0,0] cbsz:2 blgp:2
	v_mfma_scale_f32_16x16x128_f8f6f4 v[46:49], v[2:7], v[218:223], v[46:49], v160, v238 op_sel_hi:[0,0,0] cbsz:2 blgp:2
	v_mfma_scale_f32_16x16x128_f8f6f4 v[34:37], v[8:13], v[224:229], v[34:37], v156, v242 op_sel_hi:[0,0,0] cbsz:2 blgp:2
	v_mfma_scale_f32_16x16x128_f8f6f4 v[30:33], v[2:7], v[224:229], v[30:33], v160, v242 op_sel_hi:[0,0,0] cbsz:2 blgp:2
	s_setprio 0
	s_barrier
	s_add_i32 s63, s63, 2
	s_add_u32 s20, s20, 0x100
	s_addc_u32 s21, s21, 0
	s_add_u32 s61, s61, 0x100
	s_addc_u32 s62, s62, 0
	s_cmp_gt_u32 s63, 13
	s_cbranch_scc0 .LBB0_1257
	s_nop 0
	s_nop 0
	s_nop 0
	s_nop 0
	s_nop 0
	s_nop 0
	s_nop 0
	s_nop 0
	s_nop 0
	s_nop 0
	s_nop 0
	s_nop 0
	s_and_b64 vcc, exec, s[8:9]
	s_cbranch_vccz .LBB0_1260
	s_barrier

.LBB0_1279:
	ds_read_b128 v[20:23], v195
	ds_read_b128 v[166:169], v195 offset:1024
	ds_read_b128 v[14:17], v195 offset:2048
	ds_read_b128 v[162:165], v195 offset:3072
	ds_read_b128 v[8:11], v196
	ds_read_b128 v[158:161], v196 offset:1024
	ds_read_b128 v[2:5], v196 offset:2048
	ds_read_b128 v[154:157], v196 offset:3072
	s_add_u32 s24, s22, 0xfffc0080
	s_addc_u32 s25, s23, -1
	s_cmp_eq_u32 s61, 12
	s_cselect_b32 s27, s11, s25
	s_cselect_b32 s26, s49, s24
	s_cselect_b32 s25, s13, s60
	s_cselect_b32 s24, s50, s51
	s_mov_b32 m0, s46
	ds_read_b128 v[184:187], v198
	ds_read_b128 v[188:191], v198 offset:1024
	ds_read_b128 v[202:205], v198 offset:2048
	ds_read_b128 v[218:221], v198 offset:3072
	ds_read_b128 v[208:211], v198 offset:4096
	ds_read_b128 v[222:225], v198 offset:5120
	ds_read_b128 v[214:217], v198 offset:6144
	ds_read_b128 v[226:229], v198 offset:7168
	global_load_lds_dwordx4 v180, s[22:23]
	s_add_i32 m0, s21, 0xe000
	s_nop 0
	global_load_lds_dwordx4 v182, s[22:23]
	s_waitcnt vmcnt(8)
	s_waitcnt lgkmcnt(0)
	s_barrier
	s_setprio 1
	v_mov_b32_e32 v24, v166
	v_mov_b32_e32 v25, v167
	s_nop 1
	v_mfma_scale_f32_16x16x128_f8f6f4 v[150:153], v[20:25], v[184:189], v[150:153], v168, v190 op_sel_hi:[0,0,0] cbsz:2 blgp:2
	v_mov_b32_e32 v18, v162
	v_mov_b32_e32 v19, v163
	s_nop 1
	v_mfma_scale_f32_16x16x128_f8f6f4 v[138:141], v[14:19], v[184:189], v[138:141], v164, v190 op_sel_hi:[0,0,0] cbsz:2 blgp:2
	v_mov_b32_e32 v206, v218
	v_mov_b32_e32 v207, v219
	s_nop 1
	v_mfma_scale_f32_16x16x128_f8f6f4 v[134:137], v[20:25], v[202:207], v[134:137], v168, v220 op_sel_hi:[0,0,0] cbsz:2 blgp:2
	v_mfma_scale_f32_16x16x128_f8f6f4 v[122:125], v[14:19], v[202:207], v[122:125], v164, v220 op_sel_hi:[0,0,0] cbsz:2 blgp:2
	v_mov_b32_e32 v212, v222
	v_mov_b32_e32 v213, v223
	s_nop 1
	v_mfma_scale_f32_16x16x128_f8f6f4 v[118:121], v[20:25], v[208:213], v[118:121], v168, v224 op_sel_hi:[0,0,0] cbsz:2 blgp:2
	v_mfma_scale_f32_16x16x128_f8f6f4 v[106:109], v[14:19], v[208:213], v[106:109], v164, v224 op_sel_hi:[0,0,0] cbsz:2 blgp:2
	v_mov_b32_e32 v218, v226
	v_mov_b32_e32 v219, v227
	s_nop 1
	v_mfma_scale_f32_16x16x128_f8f6f4 v[102:105], v[20:25], v[214:219], v[102:105], v168, v228 op_sel_hi:[0,0,0] cbsz:2 blgp:2
	v_mfma_scale_f32_16x16x128_f8f6f4 v[90:93], v[14:19], v[214:219], v[90:93], v164, v228 op_sel_hi:[0,0,0] cbsz:2 blgp:2
	v_mov_b32_e32 v12, v158
	v_mov_b32_e32 v13, v159
	s_nop 1
	v_mfma_scale_f32_16x16x128_f8f6f4 v[146:149], v[8:13], v[184:189], v[146:149], v160, v190 op_sel_hi:[0,0,0] cbsz:2 blgp:2
	v_mov_b32_e32 v6, v154
	v_mov_b32_e32 v7, v155
	s_nop 1
	v_mfma_scale_f32_16x16x128_f8f6f4 v[142:145], v[2:7], v[184:189], v[142:145], v156, v190 op_sel_hi:[0,0,0] cbsz:2 blgp:2
	v_mfma_scale_f32_16x16x128_f8f6f4 v[130:133], v[8:13], v[202:207], v[130:133], v160, v220 op_sel_hi:[0,0,0] cbsz:2 blgp:2
	v_mfma_scale_f32_16x16x128_f8f6f4 v[126:129], v[2:7], v[202:207], v[126:129], v156, v220 op_sel_hi:[0,0,0] cbsz:2 blgp:2
	v_mfma_scale_f32_16x16x128_f8f6f4 v[114:117], v[8:13], v[208:213], v[114:117], v160, v224 op_sel_hi:[0,0,0] cbsz:2 blgp:2
	v_mfma_scale_f32_16x16x128_f8f6f4 v[110:113], v[2:7], v[208:213], v[110:113], v156, v224 op_sel_hi:[0,0,0] cbsz:2 blgp:2
	v_mfma_scale_f32_16x16x128_f8f6f4 v[98:101], v[8:13], v[214:219], v[98:101], v160, v228 op_sel_hi:[0,0,0] cbsz:2 blgp:2
	v_mfma_scale_f32_16x16x128_f8f6f4 v[94:97], v[2:7], v[214:219], v[94:97], v156, v228 op_sel_hi:[0,0,0] cbsz:2 blgp:2
	s_setprio 0
	s_barrier
	s_add_i32 s62, s42, s35
	v_lshl_add_u64 v[184:185], s[24:25], 0, v[176:177]
	s_mov_b32 m0, s62
	ds_read_b128 v[202:205], v198 offset:16384
	ds_read_b128 v[224:227], v198 offset:17408
	ds_read_b128 v[208:211], v198 offset:18432
	ds_read_b128 v[228:231], v198 offset:19456
	ds_read_b128 v[214:217], v198 offset:20480
	ds_read_b128 v[232:235], v198 offset:21504
	ds_read_b128 v[220:223], v198 offset:22528
	ds_read_b128 v[236:239], v198 offset:23552
	global_load_lds_dwordx4 v176, s[24:25]
	s_add_i32 m0, s62, 0x2000
	s_add_u32 s62, s24, 0x40000
	v_lshl_add_u64 v[186:187], s[24:25], 0, v[172:173]
	s_addc_u32 s63, s25, 0
	s_add_i32 s64, s43, s35
	global_load_lds_dwordx4 v172, s[24:25]
	s_mov_b32 m0, s64
	v_lshl_add_u64 v[188:189], s[26:27], 0, v[178:179]
	global_load_lds_dwordx4 v176, s[62:63]
	s_add_i32 m0, s64, 0x2000
	v_lshl_add_u64 v[190:191], s[26:27], 0, v[174:175]
	global_load_lds_dwordx4 v172, s[62:63]
	s_mov_b32 m0, s21
	s_nop 0
	global_load_lds_dwordx4 v178, s[26:27]
	s_mov_b32 m0, s36
	s_nop 0
	global_load_lds_dwordx4 v174, s[26:27]
	s_waitcnt vmcnt(8)
	s_waitcnt lgkmcnt(0)
	s_barrier
	s_setprio 1
	v_mov_b32_e32 v206, v224
	v_mov_b32_e32 v207, v225
	s_nop 1
	v_mfma_scale_f32_16x16x128_f8f6f4 v[86:89], v[20:25], v[202:207], v[86:89], v168, v226 op_sel_hi:[0,0,0] cbsz:2 blgp:2
	v_mfma_scale_f32_16x16x128_f8f6f4 v[74:77], v[14:19], v[202:207], v[74:77], v164, v226 op_sel_hi:[0,0,0] cbsz:2 blgp:2
	v_mov_b32_e32 v212, v228
	v_mov_b32_e32 v213, v229
	s_nop 1
	v_mfma_scale_f32_16x16x128_f8f6f4 v[70:73], v[20:25], v[208:213], v[70:73], v168, v230 op_sel_hi:[0,0,0] cbsz:2 blgp:2
	v_mfma_scale_f32_16x16x128_f8f6f4 v[58:61], v[14:19], v[208:213], v[58:61], v164, v230 op_sel_hi:[0,0,0] cbsz:2 blgp:2
	v_mov_b32_e32 v218, v232
	v_mov_b32_e32 v219, v233
	s_nop 1
	v_mfma_scale_f32_16x16x128_f8f6f4 v[54:57], v[20:25], v[214:219], v[54:57], v168, v234 op_sel_hi:[0,0,0] cbsz:2 blgp:2
	v_mfma_scale_f32_16x16x128_f8f6f4 v[42:45], v[14:19], v[214:219], v[42:45], v164, v234 op_sel_hi:[0,0,0] cbsz:2 blgp:2
	v_mov_b32_e32 v224, v236
	v_mov_b32_e32 v225, v237
	s_nop 1
	v_mfma_scale_f32_16x16x128_f8f6f4 v[38:41], v[20:25], v[220:225], v[38:41], v168, v238 op_sel_hi:[0,0,0] cbsz:2 blgp:2
	v_mfma_scale_f32_16x16x128_f8f6f4 v[26:29], v[14:19], v[220:225], v[26:29], v164, v238 op_sel_hi:[0,0,0] cbsz:2 blgp:2
	v_mfma_scale_f32_16x16x128_f8f6f4 v[82:85], v[8:13], v[202:207], v[82:85], v160, v226 op_sel_hi:[0,0,0] cbsz:2 blgp:2
	v_mfma_scale_f32_16x16x128_f8f6f4 v[78:81], v[2:7], v[202:207], v[78:81], v156, v226 op_sel_hi:[0,0,0] cbsz:2 blgp:2
	v_mfma_scale_f32_16x16x128_f8f6f4 v[66:69], v[8:13], v[208:213], v[66:69], v160, v230 op_sel_hi:[0,0,0] cbsz:2 blgp:2
	v_mfma_scale_f32_16x16x128_f8f6f4 v[62:65], v[2:7], v[208:213], v[62:65], v156, v230 op_sel_hi:[0,0,0] cbsz:2 blgp:2
	v_mfma_scale_f32_16x16x128_f8f6f4 v[50:53], v[8:13], v[214:219], v[50:53], v160, v234 op_sel_hi:[0,0,0] cbsz:2 blgp:2
	v_mfma_scale_f32_16x16x128_f8f6f4 v[46:49], v[2:7], v[214:219], v[46:49], v156, v234 op_sel_hi:[0,0,0] cbsz:2 blgp:2
	v_mfma_scale_f32_16x16x128_f8f6f4 v[34:37], v[8:13], v[220:225], v[34:37], v160, v238 op_sel_hi:[0,0,0] cbsz:2 blgp:2
	v_mfma_scale_f32_16x16x128_f8f6f4 v[30:33], v[2:7], v[220:225], v[30:33], v156, v238 op_sel_hi:[0,0,0] cbsz:2 blgp:2
	s_setprio 0
	s_barrier
	s_add_i32 s62, 0, 0x18000
	s_add_i32 s63, 0, 0x1c000
	v_add_u32_e32 v2, s62, v194
	v_add_u32_e32 v6, s63, v194
	ds_read_b128 v[20:23], v2
	ds_read_b128 v[166:169], v2 offset:1024
	ds_read_b128 v[14:17], v2 offset:2048
	ds_read_b128 v[162:165], v2 offset:3072
	ds_read_b128 v[8:11], v6
	ds_read_b128 v[154:157], v6 offset:1024
	ds_read_b128 v[2:5], v6 offset:2048
	ds_read_b128 v[158:161], v6 offset:3072
	s_add_u32 s26, s26, 0x40000
	s_addc_u32 s27, s27, 0
	s_mov_b32 m0, s37
	ds_read_b128 v[202:205], v198 offset:32768
	ds_read_b128 v[224:227], v198 offset:33792
	ds_read_b128 v[208:211], v198 offset:34816
	ds_read_b128 v[228:231], v198 offset:35840
	ds_read_b128 v[214:217], v198 offset:36864
	ds_read_b128 v[232:235], v198 offset:37888
	ds_read_b128 v[220:223], v198 offset:38912
	ds_read_b128 v[236:239], v198 offset:39936
	global_load_lds_dwordx4 v178, s[26:27]
	s_mov_b32 m0, s38
	s_nop 0
	global_load_lds_dwordx4 v174, s[26:27]
	s_waitcnt vmcnt(8)
	s_waitcnt lgkmcnt(0)
	s_barrier
	s_setprio 1
	v_mov_b32_e32 v24, v166
	v_mov_b32_e32 v25, v167
	v_mov_b32_e32 v206, v224
	v_mov_b32_e32 v207, v225
	s_nop 1
	v_mfma_scale_f32_16x16x128_f8f6f4 v[150:153], v[20:25], v[202:207], v[150:153], v168, v226 op_sel_hi:[0,0,0] cbsz:2 blgp:2
	v_mov_b32_e32 v18, v162
	v_mov_b32_e32 v19, v163
	s_nop 1
	v_mfma_scale_f32_16x16x128_f8f6f4 v[138:141], v[14:19], v[202:207], v[138:141], v164, v226 op_sel_hi:[0,0,0] cbsz:2 blgp:2
	v_mov_b32_e32 v212, v228
	v_mov_b32_e32 v213, v229
	s_nop 1
	v_mfma_scale_f32_16x16x128_f8f6f4 v[134:137], v[20:25], v[208:213], v[134:137], v168, v230 op_sel_hi:[0,0,0] cbsz:2 blgp:2
	v_mfma_scale_f32_16x16x128_f8f6f4 v[122:125], v[14:19], v[208:213], v[122:125], v164, v230 op_sel_hi:[0,0,0] cbsz:2 blgp:2
	v_mov_b32_e32 v218, v232
	v_mov_b32_e32 v219, v233
	s_nop 1
	v_mfma_scale_f32_16x16x128_f8f6f4 v[118:121], v[20:25], v[214:219], v[118:121], v168, v234 op_sel_hi:[0,0,0] cbsz:2 blgp:2
	v_mfma_scale_f32_16x16x128_f8f6f4 v[106:109], v[14:19], v[214:219], v[106:109], v164, v234 op_sel_hi:[0,0,0] cbsz:2 blgp:2
	v_mov_b32_e32 v224, v236
	v_mov_b32_e32 v225, v237
	s_nop 1
	v_mfma_scale_f32_16x16x128_f8f6f4 v[102:105], v[20:25], v[220:225], v[102:105], v168, v238 op_sel_hi:[0,0,0] cbsz:2 blgp:2
	v_mfma_scale_f32_16x16x128_f8f6f4 v[90:93], v[14:19], v[220:225], v[90:93], v164, v238 op_sel_hi:[0,0,0] cbsz:2 blgp:2
	v_mov_b32_e32 v12, v154
	v_mov_b32_e32 v13, v155
	s_nop 1
	v_mfma_scale_f32_16x16x128_f8f6f4 v[146:149], v[8:13], v[202:207], v[146:149], v156, v226 op_sel_hi:[0,0,0] cbsz:2 blgp:2
	v_mov_b32_e32 v6, v158
	v_mov_b32_e32 v7, v159
	s_nop 1
	v_mfma_scale_f32_16x16x128_f8f6f4 v[142:145], v[2:7], v[202:207], v[142:145], v160, v226 op_sel_hi:[0,0,0] cbsz:2 blgp:2
	v_mfma_scale_f32_16x16x128_f8f6f4 v[130:133], v[8:13], v[208:213], v[130:133], v156, v230 op_sel_hi:[0,0,0] cbsz:2 blgp:2
	v_mfma_scale_f32_16x16x128_f8f6f4 v[126:129], v[2:7], v[208:213], v[126:129], v160, v230 op_sel_hi:[0,0,0] cbsz:2 blgp:2
	v_mfma_scale_f32_16x16x128_f8f6f4 v[114:117], v[8:13], v[214:219], v[114:117], v156, v234 op_sel_hi:[0,0,0] cbsz:2 blgp:2
	v_mfma_scale_f32_16x16x128_f8f6f4 v[110:113], v[2:7], v[214:219], v[110:113], v160, v234 op_sel_hi:[0,0,0] cbsz:2 blgp:2
	v_mfma_scale_f32_16x16x128_f8f6f4 v[98:101], v[8:13], v[220:225], v[98:101], v156, v238 op_sel_hi:[0,0,0] cbsz:2 blgp:2
	v_mfma_scale_f32_16x16x128_f8f6f4 v[94:97], v[2:7], v[220:225], v[94:97], v160, v238 op_sel_hi:[0,0,0] cbsz:2 blgp:2
	s_setprio 0
	s_barrier
	s_add_i32 s26, s62, s35
	v_lshl_add_u64 v[154:155], v[184:185], 0, s[6:7]
	s_mov_b32 m0, s26
	ds_read_b128 v[202:205], v198 offset:49152
	ds_read_b128 v[224:227], v198 offset:50176
	ds_read_b128 v[208:211], v198 offset:51200
	ds_read_b128 v[228:231], v198 offset:52224
	ds_read_b128 v[214:217], v198 offset:53248
	ds_read_b128 v[232:235], v198 offset:54272
	ds_read_b128 v[220:223], v198 offset:55296
	ds_read_b128 v[236:239], v198 offset:56320
	global_load_lds_dwordx4 v[154:155], off
	s_add_i32 m0, s26, 0x2000
	s_add_u32 s24, s24, 0x40080
	v_lshl_add_u64 v[154:155], v[186:187], 0, s[6:7]
	s_addc_u32 s25, s25, 0
	s_add_i32 s26, s63, s35
	global_load_lds_dwordx4 v[154:155], off
	s_mov_b32 m0, s26
	s_nop 0
	global_load_lds_dwordx4 v176, s[24:25]
	s_add_i32 m0, s26, 0x2000
	s_nop 0
	global_load_lds_dwordx4 v172, s[24:25]
	v_lshl_add_u64 v[154:155], v[188:189], 0, s[6:7]
	s_mov_b32 m0, s40
	s_nop 0
	global_load_lds_dwordx4 v[154:155], off
	v_lshl_add_u64 v[154:155], v[190:191], 0, s[6:7]
	s_mov_b32 m0, s41
	s_nop 0
	global_load_lds_dwordx4 v[154:155], off
	s_waitcnt vmcnt(8)
	s_waitcnt lgkmcnt(0)
	s_barrier
	s_setprio 1
	v_mov_b32_e32 v206, v224
	v_mov_b32_e32 v207, v225
	s_nop 1
	v_mfma_scale_f32_16x16x128_f8f6f4 v[86:89], v[20:25], v[202:207], v[86:89], v168, v226 op_sel_hi:[0,0,0] cbsz:2 blgp:2
	v_mfma_scale_f32_16x16x128_f8f6f4 v[74:77], v[14:19], v[202:207], v[74:77], v164, v226 op_sel_hi:[0,0,0] cbsz:2 blgp:2
	v_mov_b32_e32 v212, v228
	v_mov_b32_e32 v213, v229
	s_nop 1
	v_mfma_scale_f32_16x16x128_f8f6f4 v[70:73], v[20:25], v[208:213], v[70:73], v168, v230 op_sel_hi:[0,0,0] cbsz:2 blgp:2
	v_mfma_scale_f32_16x16x128_f8f6f4 v[58:61], v[14:19], v[208:213], v[58:61], v164, v230 op_sel_hi:[0,0,0] cbsz:2 blgp:2
	v_mov_b32_e32 v218, v232
	v_mov_b32_e32 v219, v233
	s_nop 1
	v_mfma_scale_f32_16x16x128_f8f6f4 v[54:57], v[20:25], v[214:219], v[54:57], v168, v234 op_sel_hi:[0,0,0] cbsz:2 blgp:2
	v_mfma_scale_f32_16x16x128_f8f6f4 v[42:45], v[14:19], v[214:219], v[42:45], v164, v234 op_sel_hi:[0,0,0] cbsz:2 blgp:2
	v_mov_b32_e32 v224, v236
	v_mov_b32_e32 v225, v237
	s_nop 1
	v_mfma_scale_f32_16x16x128_f8f6f4 v[38:41], v[20:25], v[220:225], v[38:41], v168, v238 op_sel_hi:[0,0,0] cbsz:2 blgp:2
	v_mfma_scale_f32_16x16x128_f8f6f4 v[26:29], v[14:19], v[220:225], v[26:29], v164, v238 op_sel_hi:[0,0,0] cbsz:2 blgp:2
	v_mfma_scale_f32_16x16x128_f8f6f4 v[82:85], v[8:13], v[202:207], v[82:85], v156, v226 op_sel_hi:[0,0,0] cbsz:2 blgp:2
	v_mfma_scale_f32_16x16x128_f8f6f4 v[78:81], v[2:7], v[202:207], v[78:81], v160, v226 op_sel_hi:[0,0,0] cbsz:2 blgp:2
	v_mfma_scale_f32_16x16x128_f8f6f4 v[66:69], v[8:13], v[208:213], v[66:69], v156, v230 op_sel_hi:[0,0,0] cbsz:2 blgp:2
	v_mfma_scale_f32_16x16x128_f8f6f4 v[62:65], v[2:7], v[208:213], v[62:65], v160, v230 op_sel_hi:[0,0,0] cbsz:2 blgp:2
	v_mfma_scale_f32_16x16x128_f8f6f4 v[50:53], v[8:13], v[214:219], v[50:53], v156, v234 op_sel_hi:[0,0,0] cbsz:2 blgp:2
	v_mfma_scale_f32_16x16x128_f8f6f4 v[46:49], v[2:7], v[214:219], v[46:49], v160, v234 op_sel_hi:[0,0,0] cbsz:2 blgp:2
	v_mfma_scale_f32_16x16x128_f8f6f4 v[34:37], v[8:13], v[220:225], v[34:37], v156, v238 op_sel_hi:[0,0,0] cbsz:2 blgp:2
	v_mfma_scale_f32_16x16x128_f8f6f4 v[30:33], v[2:7], v[220:225], v[30:33], v160, v238 op_sel_hi:[0,0,0] cbsz:2 blgp:2
	s_setprio 0
	s_barrier
	s_add_i32 s61, s61, 2
	s_add_u32 s22, s22, 0x100
	s_addc_u32 s23, s23, 0
	s_add_u32 s51, s51, 0x100
	s_addc_u32 s60, s60, 0
	s_cmp_gt_u32 s61, 13
	s_cbranch_scc0 .LBB0_1279
	s_nop 0
	s_nop 0
	s_nop 0
	s_nop 0
	s_nop 0
	s_nop 0
	s_nop 0
	s_nop 0
	s_nop 0
	s_nop 0
	s_nop 0
	s_nop 0
	s_and_b64 vcc, exec, s[8:9]
	s_cbranch_vccz .LBB0_1282
	s_barrier

.LBB0_1391:
	ds_read_b128 v[24:27], v186
	ds_read_b128 v[28:31], v186 offset:1024
	ds_read_b128 v[16:19], v186 offset:2048
	ds_read_b128 v[20:23], v186 offset:3072
	ds_read_b128 v[8:11], v187
	ds_read_b128 v[12:15], v187 offset:1024
	ds_read_b128 v[0:3], v187 offset:2048
	ds_read_b128 v[4:7], v187 offset:3072
	s_add_u32 s26, s24, 0xfff20080
	s_addc_u32 s27, s25, -1
	s_cmp_eq_u32 s67, 52
	s_cselect_b32 s29, s23, s27
	s_cselect_b32 s28, s22, s26
	s_cselect_b32 s27, s1, s66
	s_cselect_b32 s26, s0, s65
	s_add_i32 m0, s36, 0xc000
	ds_read_b128 v[174:177], v188
	ds_read_b128 v[178:181], v188 offset:1024
	ds_read_b128 v[192:195], v188 offset:2048
	ds_read_b128 v[196:199], v188 offset:3072
	ds_read_b128 v[202:205], v188 offset:4096
	ds_read_b128 v[206:209], v188 offset:5120
	ds_read_b128 v[210:213], v188 offset:6144
	ds_read_b128 v[214:217], v188 offset:7168
	global_load_lds_dwordx4 v170, s[24:25]
	s_add_i32 m0, s36, 0xe000
	s_nop 0
	global_load_lds_dwordx4 v172, s[24:25]
	s_waitcnt vmcnt(8)
	s_waitcnt lgkmcnt(0)
	s_barrier
	s_setprio 1
	v_mfma_scale_f32_16x16x128_f8f6f4 v[156:159], v[24:31], v[174:181], v[156:159], v189, v190 op_sel_hi:[0,0,0]
	v_mfma_scale_f32_16x16x128_f8f6f4 v[152:155], v[16:23], v[174:181], v[152:155], v189, v190 op_sel_hi:[0,0,0]
	v_mfma_scale_f32_16x16x128_f8f6f4 v[140:143], v[24:31], v[192:199], v[140:143], v189, v190 op_sel_hi:[0,0,0]
	v_mfma_scale_f32_16x16x128_f8f6f4 v[136:139], v[16:23], v[192:199], v[136:139], v189, v190 op_sel_hi:[0,0,0]
	v_mfma_scale_f32_16x16x128_f8f6f4 v[124:127], v[24:31], v[202:209], v[124:127], v189, v190 op_sel_hi:[0,0,0]
	v_mfma_scale_f32_16x16x128_f8f6f4 v[120:123], v[16:23], v[202:209], v[120:123], v189, v190 op_sel_hi:[0,0,0]
	v_mfma_scale_f32_16x16x128_f8f6f4 v[108:111], v[24:31], v[210:217], v[108:111], v189, v190 op_sel_hi:[0,0,0]
	v_mfma_scale_f32_16x16x128_f8f6f4 v[104:107], v[16:23], v[210:217], v[104:107], v189, v190 op_sel_hi:[0,0,0]
	v_mfma_scale_f32_16x16x128_f8f6f4 v[148:151], v[8:15], v[174:181], v[148:151], v189, v190 op_sel_hi:[0,0,0]
	v_mfma_scale_f32_16x16x128_f8f6f4 v[144:147], v[0:7], v[174:181], v[144:147], v189, v190 op_sel_hi:[0,0,0]
	v_mfma_scale_f32_16x16x128_f8f6f4 v[132:135], v[8:15], v[192:199], v[132:135], v189, v190 op_sel_hi:[0,0,0]
	v_mfma_scale_f32_16x16x128_f8f6f4 v[128:131], v[0:7], v[192:199], v[128:131], v189, v190 op_sel_hi:[0,0,0]
	v_mfma_scale_f32_16x16x128_f8f6f4 v[116:119], v[8:15], v[202:209], v[116:119], v189, v190 op_sel_hi:[0,0,0]
	v_mfma_scale_f32_16x16x128_f8f6f4 v[112:115], v[0:7], v[202:209], v[112:115], v189, v190 op_sel_hi:[0,0,0]
	v_mfma_scale_f32_16x16x128_f8f6f4 v[100:103], v[8:15], v[210:217], v[100:103], v189, v190 op_sel_hi:[0,0,0]
	v_mfma_scale_f32_16x16x128_f8f6f4 v[96:99], v[0:7], v[210:217], v[96:99], v189, v190 op_sel_hi:[0,0,0]
	s_setprio 0
	s_barrier
	s_add_i32 s68, s44, s35
	v_lshl_add_u64 v[174:175], s[26:27], 0, v[160:161]
	s_mov_b32 m0, s68
	ds_read_b128 v[192:195], v188 offset:16384
	ds_read_b128 v[196:199], v188 offset:17408
	ds_read_b128 v[202:205], v188 offset:18432
	ds_read_b128 v[206:209], v188 offset:19456
	ds_read_b128 v[210:213], v188 offset:20480
	ds_read_b128 v[214:217], v188 offset:21504
	ds_read_b128 v[218:221], v188 offset:22528
	ds_read_b128 v[222:225], v188 offset:23552
	global_load_lds_dwordx4 v160, s[26:27]
	s_add_i32 m0, s68, 0x2000
	s_add_u32 s68, s26, 0xe0000
	v_lshl_add_u64 v[176:177], s[26:27], 0, v[164:165]
	s_addc_u32 s69, s27, 0
	s_add_i32 s70, s45, s35
	global_load_lds_dwordx4 v164, s[26:27]
	s_mov_b32 m0, s70
	v_lshl_add_u64 v[180:181], s[28:29], 0, v[166:167]
	global_load_lds_dwordx4 v160, s[68:69]
	s_add_i32 m0, s70, 0x2000
	s_nop 0
	global_load_lds_dwordx4 v164, s[68:69]
	v_lshl_add_u64 v[178:179], s[28:29], 0, v[168:169]
	s_mov_b32 m0, s36
	s_nop 0
	global_load_lds_dwordx4 v168, s[28:29]
	s_mov_b32 m0, s37
	s_nop 0
	global_load_lds_dwordx4 v166, s[28:29]
	s_waitcnt vmcnt(8)
	s_waitcnt lgkmcnt(0)
	s_barrier
	s_setprio 1
	v_mfma_scale_f32_16x16x128_f8f6f4 v[92:95], v[24:31], v[192:199], v[92:95], v189, v190 op_sel_hi:[0,0,0]
	v_mfma_scale_f32_16x16x128_f8f6f4 v[88:91], v[16:23], v[192:199], v[88:91], v189, v190 op_sel_hi:[0,0,0]
	v_mfma_scale_f32_16x16x128_f8f6f4 v[76:79], v[24:31], v[202:209], v[76:79], v189, v190 op_sel_hi:[0,0,0]
	v_mfma_scale_f32_16x16x128_f8f6f4 v[72:75], v[16:23], v[202:209], v[72:75], v189, v190 op_sel_hi:[0,0,0]
	v_mfma_scale_f32_16x16x128_f8f6f4 v[60:63], v[24:31], v[210:217], v[60:63], v189, v190 op_sel_hi:[0,0,0]
	v_mfma_scale_f32_16x16x128_f8f6f4 v[56:59], v[16:23], v[210:217], v[56:59], v189, v190 op_sel_hi:[0,0,0]
	v_mfma_scale_f32_16x16x128_f8f6f4 v[44:47], v[24:31], v[218:225], v[44:47], v189, v190 op_sel_hi:[0,0,0]
	v_mfma_scale_f32_16x16x128_f8f6f4 v[40:43], v[16:23], v[218:225], v[40:43], v189, v190 op_sel_hi:[0,0,0]
	v_mfma_scale_f32_16x16x128_f8f6f4 v[84:87], v[8:15], v[192:199], v[84:87], v189, v190 op_sel_hi:[0,0,0]
	v_mfma_scale_f32_16x16x128_f8f6f4 v[80:83], v[0:7], v[192:199], v[80:83], v189, v190 op_sel_hi:[0,0,0]
	v_mfma_scale_f32_16x16x128_f8f6f4 v[68:71], v[8:15], v[202:209], v[68:71], v189, v190 op_sel_hi:[0,0,0]
	v_mfma_scale_f32_16x16x128_f8f6f4 v[64:67], v[0:7], v[202:209], v[64:67], v189, v190 op_sel_hi:[0,0,0]
	v_mfma_scale_f32_16x16x128_f8f6f4 v[52:55], v[8:15], v[210:217], v[52:55], v189, v190 op_sel_hi:[0,0,0]
	v_mfma_scale_f32_16x16x128_f8f6f4 v[48:51], v[0:7], v[210:217], v[48:51], v189, v190 op_sel_hi:[0,0,0]
	v_mfma_scale_f32_16x16x128_f8f6f4 v[36:39], v[8:15], v[218:225], v[36:39], v189, v190 op_sel_hi:[0,0,0]
	v_mfma_scale_f32_16x16x128_f8f6f4 v[32:35], v[0:7], v[218:225], v[32:35], v189, v190 op_sel_hi:[0,0,0]
	s_setprio 0
	s_barrier
	s_add_i32 s68, 0, 0x18000
	s_add_i32 s69, 0, 0x1c000
	v_add_u32_e32 v12, s68, v184
	v_add_u32_e32 v28, s69, v184
	ds_read_b128 v[0:3], v12
	ds_read_b128 v[4:7], v12 offset:1024
	ds_read_b128 v[8:11], v12 offset:2048
	ds_read_b128 v[12:15], v12 offset:3072
	ds_read_b128 v[16:19], v28
	ds_read_b128 v[20:23], v28 offset:1024
	ds_read_b128 v[24:27], v28 offset:2048
	ds_read_b128 v[28:31], v28 offset:3072
	s_add_u32 s28, s28, 0xe0000
	s_addc_u32 s29, s29, 0
	s_mov_b32 m0, s38
	ds_read_b128 v[192:195], v188 offset:32768
	ds_read_b128 v[196:199], v188 offset:33792
	ds_read_b128 v[202:205], v188 offset:34816
	ds_read_b128 v[206:209], v188 offset:35840
	ds_read_b128 v[210:213], v188 offset:36864
	ds_read_b128 v[214:217], v188 offset:37888
	ds_read_b128 v[218:221], v188 offset:38912
	ds_read_b128 v[222:225], v188 offset:39936
	global_load_lds_dwordx4 v168, s[28:29]
	s_mov_b32 m0, s39
	s_nop 0
	global_load_lds_dwordx4 v166, s[28:29]
	s_waitcnt vmcnt(8)
	s_waitcnt lgkmcnt(0)
	s_barrier
	s_setprio 1
	v_mfma_scale_f32_16x16x128_f8f6f4 v[156:159], v[0:7], v[192:199], v[156:159], v189, v190 op_sel_hi:[0,0,0]
	v_mfma_scale_f32_16x16x128_f8f6f4 v[152:155], v[8:15], v[192:199], v[152:155], v189, v190 op_sel_hi:[0,0,0]
	v_mfma_scale_f32_16x16x128_f8f6f4 v[140:143], v[0:7], v[202:209], v[140:143], v189, v190 op_sel_hi:[0,0,0]
	v_mfma_scale_f32_16x16x128_f8f6f4 v[136:139], v[8:15], v[202:209], v[136:139], v189, v190 op_sel_hi:[0,0,0]
	v_mfma_scale_f32_16x16x128_f8f6f4 v[124:127], v[0:7], v[210:217], v[124:127], v189, v190 op_sel_hi:[0,0,0]
	v_mfma_scale_f32_16x16x128_f8f6f4 v[120:123], v[8:15], v[210:217], v[120:123], v189, v190 op_sel_hi:[0,0,0]
	v_mfma_scale_f32_16x16x128_f8f6f4 v[108:111], v[0:7], v[218:225], v[108:111], v189, v190 op_sel_hi:[0,0,0]
	v_mfma_scale_f32_16x16x128_f8f6f4 v[104:107], v[8:15], v[218:225], v[104:107], v189, v190 op_sel_hi:[0,0,0]
	v_mfma_scale_f32_16x16x128_f8f6f4 v[148:151], v[16:23], v[192:199], v[148:151], v189, v190 op_sel_hi:[0,0,0]
	v_mfma_scale_f32_16x16x128_f8f6f4 v[144:147], v[24:31], v[192:199], v[144:147], v189, v190 op_sel_hi:[0,0,0]
	v_mfma_scale_f32_16x16x128_f8f6f4 v[132:135], v[16:23], v[202:209], v[132:135], v189, v190 op_sel_hi:[0,0,0]
	v_mfma_scale_f32_16x16x128_f8f6f4 v[128:131], v[24:31], v[202:209], v[128:131], v189, v190 op_sel_hi:[0,0,0]
	v_mfma_scale_f32_16x16x128_f8f6f4 v[116:119], v[16:23], v[210:217], v[116:119], v189, v190 op_sel_hi:[0,0,0]
	v_mfma_scale_f32_16x16x128_f8f6f4 v[112:115], v[24:31], v[210:217], v[112:115], v189, v190 op_sel_hi:[0,0,0]
	v_mfma_scale_f32_16x16x128_f8f6f4 v[100:103], v[16:23], v[218:225], v[100:103], v189, v190 op_sel_hi:[0,0,0]
	v_mfma_scale_f32_16x16x128_f8f6f4 v[96:99], v[24:31], v[218:225], v[96:99], v189, v190 op_sel_hi:[0,0,0]
	s_setprio 0
	s_barrier
	s_add_i32 s28, s68, s35
	v_lshl_add_u64 v[174:175], v[174:175], 0, s[8:9]
	s_mov_b32 m0, s28
	ds_read_b128 v[192:195], v188 offset:49152
	ds_read_b128 v[196:199], v188 offset:50176
	ds_read_b128 v[202:205], v188 offset:51200
	ds_read_b128 v[206:209], v188 offset:52224
	ds_read_b128 v[210:213], v188 offset:53248
	ds_read_b128 v[214:217], v188 offset:54272
	ds_read_b128 v[218:221], v188 offset:55296
	ds_read_b128 v[222:225], v188 offset:56320
	global_load_lds_dwordx4 v[174:175], off
	s_add_i32 m0, s28, 0x2000
	s_add_u32 s26, s26, 0xe0080
	v_lshl_add_u64 v[174:175], v[176:177], 0, s[8:9]
	s_addc_u32 s27, s27, 0
	s_add_i32 s28, s69, s35
	global_load_lds_dwordx4 v[174:175], off
	s_mov_b32 m0, s28
	s_nop 0
	global_load_lds_dwordx4 v160, s[26:27]
	s_add_i32 m0, s28, 0x2000
	s_nop 0
	global_load_lds_dwordx4 v164, s[26:27]
	v_lshl_add_u64 v[174:175], v[178:179], 0, s[8:9]
	s_mov_b32 m0, s41
	s_nop 0
	global_load_lds_dwordx4 v[174:175], off
	v_lshl_add_u64 v[174:175], v[180:181], 0, s[8:9]
	s_mov_b32 m0, s42
	s_nop 0
	global_load_lds_dwordx4 v[174:175], off
	s_waitcnt vmcnt(8)
	s_waitcnt lgkmcnt(0)
	s_barrier
	s_setprio 1
	v_mfma_scale_f32_16x16x128_f8f6f4 v[92:95], v[0:7], v[192:199], v[92:95], v189, v190 op_sel_hi:[0,0,0]
	v_mfma_scale_f32_16x16x128_f8f6f4 v[88:91], v[8:15], v[192:199], v[88:91], v189, v190 op_sel_hi:[0,0,0]
	v_mfma_scale_f32_16x16x128_f8f6f4 v[76:79], v[0:7], v[202:209], v[76:79], v189, v190 op_sel_hi:[0,0,0]
	v_mfma_scale_f32_16x16x128_f8f6f4 v[72:75], v[8:15], v[202:209], v[72:75], v189, v190 op_sel_hi:[0,0,0]
	v_mfma_scale_f32_16x16x128_f8f6f4 v[60:63], v[0:7], v[210:217], v[60:63], v189, v190 op_sel_hi:[0,0,0]
	v_mfma_scale_f32_16x16x128_f8f6f4 v[56:59], v[8:15], v[210:217], v[56:59], v189, v190 op_sel_hi:[0,0,0]
	v_mfma_scale_f32_16x16x128_f8f6f4 v[44:47], v[0:7], v[218:225], v[44:47], v189, v190 op_sel_hi:[0,0,0]
	v_mfma_scale_f32_16x16x128_f8f6f4 v[40:43], v[8:15], v[218:225], v[40:43], v189, v190 op_sel_hi:[0,0,0]
	v_mfma_scale_f32_16x16x128_f8f6f4 v[84:87], v[16:23], v[192:199], v[84:87], v189, v190 op_sel_hi:[0,0,0]
	v_mfma_scale_f32_16x16x128_f8f6f4 v[80:83], v[24:31], v[192:199], v[80:83], v189, v190 op_sel_hi:[0,0,0]
	v_mfma_scale_f32_16x16x128_f8f6f4 v[68:71], v[16:23], v[202:209], v[68:71], v189, v190 op_sel_hi:[0,0,0]
	v_mfma_scale_f32_16x16x128_f8f6f4 v[64:67], v[24:31], v[202:209], v[64:67], v189, v190 op_sel_hi:[0,0,0]
	v_mfma_scale_f32_16x16x128_f8f6f4 v[52:55], v[16:23], v[210:217], v[52:55], v189, v190 op_sel_hi:[0,0,0]
	v_mfma_scale_f32_16x16x128_f8f6f4 v[48:51], v[24:31], v[210:217], v[48:51], v189, v190 op_sel_hi:[0,0,0]
	v_mfma_scale_f32_16x16x128_f8f6f4 v[36:39], v[16:23], v[218:225], v[36:39], v189, v190 op_sel_hi:[0,0,0]
	v_mfma_scale_f32_16x16x128_f8f6f4 v[32:35], v[24:31], v[218:225], v[32:35], v189, v190 op_sel_hi:[0,0,0]
	s_setprio 0
	s_barrier
	s_add_i32 s67, s67, 2
	s_add_u32 s24, s24, 0x100
	s_addc_u32 s25, s25, 0
	s_add_u32 s65, s65, 0x100
	s_addc_u32 s66, s66, 0
	s_cmp_gt_u32 s67, 53
	s_cbranch_scc0 .LBB0_1391
	s_nop 0
	s_nop 0
	s_nop 0
	s_nop 0
	s_nop 0
	s_nop 0
	s_nop 0
	s_nop 0
	s_nop 0
	s_nop 0
	s_nop 0
	s_nop 0
	s_and_b64 vcc, exec, s[10:11]
	s_cbranch_vccz .LBB0_1394
	s_barrier
